# baseline (speedup 1.0000x reference)
.LBB2_24:
	s_or_b64 exec, exec, s[0:1]
	v_and_b32_e32 v1, 31, v0
	v_lshrrev_b32_e32 v158, 5, v156
	s_waitcnt lgkmcnt(0)
	s_barrier
	v_lshlrev_b32_e32 v250, 4, v158
	v_lshl_or_b32 v250, s10, 7, v250
	v_or_b32_e32 v254, 0x1ee00, v250
	ds_read_b128 v[168:171], v254 offset:0
	ds_read_b128 v[172:175], v254 offset:32
	ds_read_b128 v[176:179], v254 offset:64
	ds_read_b128 v[180:183], v254 offset:96
	v_bfe_u32 v255, v156, 2, 2
	v_lshl_add_u32 v250, v255, 2, v250
	v_add_u32_e32 v250, 0x1e400, v250
	s_waitcnt lgkmcnt(0)
	s_barrier
	v_mul_u32_u24_e32 v2, 0x88, v1
	s_mul_i32 s0, s11, 0x4400
	v_lshlrev_b32_e32 v2, 1, v2
	v_lshlrev_b32_e32 v3, 4, v158
	v_mov_b32_e32 v138, v0
	v_add3_u32 v159, s0, v2, v3
	ds_read_b128 v[2:5], v159
	ds_read_b128 v[18:21], v159 offset:8704
	ds_read_b128 v[130:133], v159 offset:32
	s_waitcnt vmcnt(10) lgkmcnt(2)
	v_mfma_f32_32x32x16_f16 v[50:65], v[2:5], v[126:129], 0
	s_mov_b32 s4, 0xc060c00
	s_mov_b32 s5, 0xe400
	s_mulk_i32 s11, 0x2400
	s_lshl_b32 s0, s10, 6
	s_or_b32 s0, s11, s0
	s_add_i32 s0, s0, 0x11000
	v_mul_u32_u24_e32 v251, 0x90, v1
	v_lshl_add_u32 v251, v158, 3, v251
	v_add_u32_e32 v251, s0, v251
	s_waitcnt lgkmcnt(1)
	v_mfma_f32_32x32x16_f16 v[34:49], v[18:21], v[126:129], 0
	s_or_b32 s0, s8, 2
	s_ashr_i32 s1, s0, 31
	s_lshl_b64 s[0:1], s[0:1], 12
	s_add_u32 s0, s2, s0
	s_addc_u32 s1, s3, s1
	v_cmp_gt_u32_e32 vcc, 32, v156
	v_mfma_f32_32x32x16_f16 v[2:17], v[122:125], v[2:5], v[168:183]
	v_mfma_f32_32x32x16_f16 v[18:33], v[122:125], v[18:21], v[168:183]
	ds_read_b128 v[134:137], v159 offset:8736
	ds_read_b128 v[160:163], v159 offset:64
	s_waitcnt vmcnt(8) lgkmcnt(2)
	v_mfma_f32_32x32x16_f16 v[50:65], v[130:133], v[118:121], v[50:65]
	s_waitcnt lgkmcnt(1)
	v_mfma_f32_32x32x16_f16 v[34:49], v[134:137], v[118:121], v[34:49]
	v_mfma_f32_32x32x16_f16 v[2:17], v[114:117], v[130:133], v[2:17]
	v_mfma_f32_32x32x16_f16 v[18:33], v[114:117], v[134:137], v[18:33]
	ds_read_b128 v[130:133], v159 offset:8768
	ds_read_b128 v[134:137], v159 offset:96
	s_waitcnt vmcnt(6) lgkmcnt(2)
	v_mfma_f32_32x32x16_f16 v[50:65], v[160:163], v[110:113], v[50:65]
	s_waitcnt lgkmcnt(1)
	v_mfma_f32_32x32x16_f16 v[34:49], v[130:133], v[110:113], v[34:49]
	v_mfma_f32_32x32x16_f16 v[2:17], v[106:109], v[160:163], v[2:17]
	v_mfma_f32_32x32x16_f16 v[18:33], v[106:109], v[130:133], v[18:33]
	ds_read_b128 v[130:133], v159 offset:8800
	ds_read_b128 v[160:163], v159 offset:128
	s_waitcnt vmcnt(4) lgkmcnt(2)
	v_mfma_f32_32x32x16_f16 v[50:65], v[134:137], v[102:105], v[50:65]
	s_waitcnt lgkmcnt(1)
	v_mfma_f32_32x32x16_f16 v[34:49], v[130:133], v[102:105], v[34:49]
	v_mfma_f32_32x32x16_f16 v[2:17], v[98:101], v[134:137], v[2:17]
	v_mfma_f32_32x32x16_f16 v[18:33], v[98:101], v[130:133], v[18:33]
	ds_read_b128 v[130:133], v159 offset:8832
	ds_read_b128 v[134:137], v159 offset:160
	s_waitcnt vmcnt(3) lgkmcnt(2)
	v_mfma_f32_32x32x16_f16 v[50:65], v[160:163], v[94:97], v[50:65]
	s_waitcnt lgkmcnt(1)
	v_mfma_f32_32x32x16_f16 v[34:49], v[130:133], v[94:97], v[34:49]
	v_mfma_f32_32x32x16_f16 v[2:17], v[86:89], v[160:163], v[2:17]
	v_mfma_f32_32x32x16_f16 v[18:33], v[86:89], v[130:133], v[18:33]
	ds_read_b128 v[130:133], v159 offset:8864
	ds_read_b128 v[160:163], v159 offset:192
	s_waitcnt vmcnt(2) lgkmcnt(2)
	v_mfma_f32_32x32x16_f16 v[50:65], v[134:137], v[90:93], v[50:65]
	s_waitcnt lgkmcnt(1)
	v_mfma_f32_32x32x16_f16 v[34:49], v[130:133], v[90:93], v[34:49]
	v_mfma_f32_32x32x16_f16 v[2:17], v[78:81], v[134:137], v[2:17]
	v_mfma_f32_32x32x16_f16 v[18:33], v[78:81], v[130:133], v[18:33]
	ds_read_b128 v[130:133], v159 offset:8896
	ds_read_b128 v[164:167], v159 offset:224
	s_waitcnt vmcnt(1) lgkmcnt(2)
	v_mfma_f32_32x32x16_f16 v[50:65], v[160:163], v[82:85], v[50:65]
	s_waitcnt lgkmcnt(1)
	v_mfma_f32_32x32x16_f16 v[34:49], v[130:133], v[82:85], v[34:49]
	v_mfma_f32_32x32x16_f16 v[2:17], v[70:73], v[160:163], v[2:17]
	v_mfma_f32_32x32x16_f16 v[18:33], v[70:73], v[130:133], v[18:33]
	v_lshlrev_b32_e32 v130, 3, v138
	v_and_b32_e32 v241, 0x1f8, v130
	global_load_dwordx2 v[138:139], v241, s[0:1]
	global_load_dwordx2 v[134:135], v241, s[0:1] offset:512
	global_load_dwordx2 v[132:133], v241, s[0:1] offset:1024
	global_load_dwordx2 v[130:131], v241, s[0:1] offset:1536
	global_load_dwordx2 v[136:137], v241, s[0:1] offset:2048
	s_waitcnt vmcnt(5) lgkmcnt(0)
	v_mfma_f32_32x32x16_f16 v[50:65], v[164:167], v[74:77], v[50:65]
	v_mfma_f32_32x32x16_f16 v[2:17], v[66:69], v[164:167], v[2:17]
	s_nop 10
	v_cvt_pk_f16_f32 v57, v56, v57
	v_cvt_pk_f16_f32 v56, v54, v55
	v_cvt_pk_f16_f32 v55, v52, v53
	v_cvt_pk_f16_f32 v54, v50, v51
	v_perm_b32 v50, v240, v154, s42
	v_perm_b32 v51, v240, v154, s43
	v_perm_b32 v52, v240, v155, s42
	v_perm_b32 v53, v240, v155, s43
	v_pk_add_f16 v50, v50, s5 op_sel_hi:[1,0]
	v_pk_add_f16 v51, v51, s5 op_sel_hi:[1,0]
	v_pk_add_f16 v52, v52, s5 op_sel_hi:[1,0]
	v_pk_add_f16 v53, v53, s5 op_sel_hi:[1,0]
	v_cvt_pk_f16_f32 v65, v64, v65
	v_cvt_pk_f16_f32 v64, v62, v63
	v_cvt_pk_f16_f32 v63, v60, v61
	v_cvt_pk_f16_f32 v62, v58, v59
	v_mfma_f32_32x32x16_f16 v[2:17], v[54:57], v[50:53], v[2:17]
	v_perm_b32 v58, v240, v150, s42
	v_perm_b32 v59, v240, v150, s43
	v_perm_b32 v60, v240, v151, s42
	v_perm_b32 v61, v240, v151, s43
	v_pk_add_f16 v58, v58, s5 op_sel_hi:[1,0]
	v_pk_add_f16 v59, v59, s5 op_sel_hi:[1,0]
	v_pk_add_f16 v60, v60, s5 op_sel_hi:[1,0]
	v_pk_add_f16 v61, v61, s5 op_sel_hi:[1,0]
	s_nop 1
	v_mfma_f32_32x32x16_f16 v[2:17], v[62:65], v[58:61], v[2:17]
	ds_read_b128 v[160:163], v159 offset:8928
	v_perm_b32 v155, v240, v152, s43
	v_perm_b32 v164, v240, v153, s42
	s_waitcnt lgkmcnt(0)
	v_mfma_f32_32x32x16_f16 v[18:33], v[66:69], v[160:163], v[18:33]
	v_perm_b32 v154, v240, v152, s42
	v_perm_b32 v165, v240, v153, s43
	v_pk_add_f16 v152, v154, s5 op_sel_hi:[1,0]
	v_pk_add_f16 v153, v155, s5 op_sel_hi:[1,0]
	v_pk_add_f16 v154, v164, s5 op_sel_hi:[1,0]
	v_pk_add_f16 v155, v165, s5 op_sel_hi:[1,0]
	v_mfma_f32_32x32x16_f16 v[34:49], v[160:163], v[74:77], v[34:49]
	v_perm_b32 v151, v240, v148, s43
	v_perm_b32 v164, v240, v149, s42
	v_mfma_f32_32x32x16_f16 v[18:33], v[54:57], v[152:155], v[18:33]
	v_perm_b32 v150, v240, v148, s42
	v_perm_b32 v165, v240, v149, s43
	v_pk_add_f16 v148, v150, s5 op_sel_hi:[1,0]
	v_pk_add_f16 v149, v151, s5 op_sel_hi:[1,0]
	v_pk_add_f16 v150, v164, s5 op_sel_hi:[1,0]
	v_pk_add_f16 v151, v165, s5 op_sel_hi:[1,0]
	s_nop 2
	v_cvt_pk_f16_f32 v41, v40, v41
	v_cvt_pk_f16_f32 v40, v38, v39
	v_cvt_pk_f16_f32 v38, v34, v35
	v_cvt_pk_f16_f32 v39, v36, v37
	v_mfma_f32_32x32x16_f16 v[18:33], v[62:65], v[148:151], v[18:33]
	v_perm_b32 v34, v240, v146, s42
	v_perm_b32 v35, v240, v146, s43
	v_perm_b32 v36, v240, v147, s42
	v_perm_b32 v37, v240, v147, s43
	v_pk_add_f16 v34, v34, s5 op_sel_hi:[1,0]
	v_pk_add_f16 v35, v35, s5 op_sel_hi:[1,0]
	v_pk_add_f16 v36, v36, s5 op_sel_hi:[1,0]
	v_pk_add_f16 v37, v37, s5 op_sel_hi:[1,0]
	v_perm_b32 v146, v240, v144, s42
	v_perm_b32 v144, v240, v144, s43
	v_perm_b32 v147, v240, v145, s42
	v_perm_b32 v53, v240, v145, s43
	v_pk_add_f16 v50, v146, s5 op_sel_hi:[1,0]
	v_pk_add_f16 v51, v144, s5 op_sel_hi:[1,0]
	v_pk_add_f16 v52, v147, s5 op_sel_hi:[1,0]
	v_pk_add_f16 v53, v53, s5 op_sel_hi:[1,0]
	v_cvt_pk_f16_f32 v49, v48, v49
	v_cvt_pk_f16_f32 v48, v46, v47
	v_cvt_pk_f16_f32 v47, v44, v45
	v_mfma_f32_32x32x16_f16 v[2:17], v[38:41], v[34:37], v[2:17]
	v_cvt_pk_f16_f32 v46, v42, v43
	v_mfma_f32_32x32x16_f16 v[18:33], v[38:41], v[50:53], v[18:33]
	v_perm_b32 v34, v240, v140, s42
	v_perm_b32 v35, v240, v140, s43
	v_perm_b32 v36, v240, v141, s42
	v_perm_b32 v37, v240, v141, s43
	v_perm_b32 v42, v240, v142, s42
	v_perm_b32 v43, v240, v142, s43
	v_perm_b32 v44, v240, v143, s42
	v_perm_b32 v45, v240, v143, s43
	v_pk_add_f16 v34, v34, s5 op_sel_hi:[1,0]
	v_pk_add_f16 v35, v35, s5 op_sel_hi:[1,0]
	v_pk_add_f16 v36, v36, s5 op_sel_hi:[1,0]
	v_pk_add_f16 v37, v37, s5 op_sel_hi:[1,0]
	v_pk_add_f16 v42, v42, s5 op_sel_hi:[1,0]
	v_pk_add_f16 v43, v43, s5 op_sel_hi:[1,0]
	v_pk_add_f16 v44, v44, s5 op_sel_hi:[1,0]
	v_pk_add_f16 v45, v45, s5 op_sel_hi:[1,0]
	v_mfma_f32_32x32x16_f16 v[18:33], v[46:49], v[34:37], v[18:33]
	global_load_dwordx2 v[154:155], v241, s[0:1] offset:2560
	global_load_dwordx2 v[152:153], v241, s[0:1] offset:3072
	global_load_dwordx2 v[150:151], v241, s[0:1] offset:3584
	v_mov_b32_e32 v148, v0
	s_or_b32 s0, s8, 4
	s_ashr_i32 s1, s0, 31
	s_lshl_b64 s[0:1], s[0:1], 12
	v_mfma_f32_32x32x16_f16 v[2:17], v[46:49], v[42:45], v[2:17]
	s_nop 7
	s_nop 4
	v_cvt_pk_f16_f32 v254, v2, v3
	v_cvt_pk_f16_f32 v255, v4, v5
	ds_write_b64 v251, v[254:255] offset:0
	v_cvt_pk_f16_f32 v252, v6, v7
	v_cvt_pk_f16_f32 v253, v8, v9
	ds_write_b64 v251, v[252:253] offset:16
	v_cvt_pk_f16_f32 v254, v10, v11
	v_cvt_pk_f16_f32 v255, v12, v13
	ds_write_b64 v251, v[254:255] offset:32
	v_cvt_pk_f16_f32 v252, v14, v15
	v_cvt_pk_f16_f32 v253, v16, v17
	ds_write_b64 v251, v[252:253] offset:48
	v_cvt_pk_f16_f32 v254, v18, v19
	v_cvt_pk_f16_f32 v255, v20, v21
	ds_write_b64 v251, v[254:255] offset:4608
	v_pk_add_f32 v[222:223], v[2:3], v[18:19]
	v_pk_mul_f32 v[194:195], v[2:3], v[2:3]
	v_pk_fma_f32 v[194:195], v[18:19], v[18:19], v[194:195]
	v_pk_add_f32 v[220:221], v[4:5], v[20:21]
	v_pk_mul_f32 v[192:193], v[4:5], v[4:5]
	v_pk_fma_f32 v[192:193], v[20:21], v[20:21], v[192:193]
	v_cvt_pk_f16_f32 v252, v22, v23
	v_cvt_pk_f16_f32 v253, v24, v25
	ds_write_b64 v251, v[252:253] offset:4624
	v_pk_add_f32 v[218:219], v[6:7], v[22:23]
	v_pk_mul_f32 v[184:185], v[6:7], v[6:7]
	v_pk_fma_f32 v[184:185], v[22:23], v[22:23], v[184:185]
	v_pk_add_f32 v[216:217], v[8:9], v[24:25]
	v_pk_mul_f32 v[166:167], v[8:9], v[8:9]
	v_pk_fma_f32 v[166:167], v[24:25], v[24:25], v[166:167]
	v_cvt_pk_f16_f32 v254, v26, v27
	v_cvt_pk_f16_f32 v255, v28, v29
	ds_write_b64 v251, v[254:255] offset:4640
	v_pk_add_f32 v[214:215], v[10:11], v[26:27]
	v_pk_mul_f32 v[164:165], v[10:11], v[10:11]
	v_pk_fma_f32 v[164:165], v[26:27], v[26:27], v[164:165]
	v_pk_add_f32 v[204:205], v[12:13], v[28:29]
	v_pk_mul_f32 v[162:163], v[12:13], v[12:13]
	v_pk_fma_f32 v[162:163], v[28:29], v[28:29], v[162:163]
	v_cvt_pk_f16_f32 v252, v30, v31
	v_cvt_pk_f16_f32 v253, v32, v33
	ds_write_b64 v251, v[252:253] offset:4656
	v_pk_add_f32 v[202:203], v[14:15], v[30:31]
	v_pk_mul_f32 v[160:161], v[14:15], v[14:15]
	v_pk_fma_f32 v[160:161], v[30:31], v[30:31], v[160:161]
	v_pk_add_f32 v[196:197], v[16:17], v[32:33]
	v_pk_mul_f32 v[156:157], v[16:17], v[16:17]
	v_pk_fma_f32 v[156:157], v[32:33], v[32:33], v[156:157]
	s_nop 3
	s_nop 0
	s_waitcnt lgkmcnt(0)
	s_barrier
	s_nop 4
	ds_read_b128 v[2:5], v159 offset:34816
	ds_read_b128 v[18:21], v159 offset:43520
	ds_read_b128 v[140:143], v159 offset:34848
	ds_read_b128 v[144:147], v159 offset:43552
	s_waitcnt lgkmcnt(3)
	v_mfma_f32_32x32x16_f16 v[50:65], v[2:5], v[126:129], 0
	s_add_u32 s0, s2, s0
	s_addc_u32 s1, s3, s1
	s_waitcnt lgkmcnt(2)
	v_mfma_f32_32x32x16_f16 v[34:49], v[18:21], v[126:129], 0
	v_mfma_f32_32x32x16_f16 v[2:17], v[122:125], v[2:5], v[168:183]
	v_mfma_f32_32x32x16_f16 v[18:33], v[122:125], v[18:21], v[168:183]
	ds_read_b128 v[242:245], v159 offset:34880
	ds_read_b128 v[246:249], v159 offset:43584
	s_waitcnt lgkmcnt(3)
	v_mfma_f32_32x32x16_f16 v[50:65], v[140:143], v[118:121], v[50:65]
	s_waitcnt lgkmcnt(2)
	v_mfma_f32_32x32x16_f16 v[34:49], v[144:147], v[118:121], v[34:49]
	v_mfma_f32_32x32x16_f16 v[2:17], v[114:117], v[140:143], v[2:17]
	v_mfma_f32_32x32x16_f16 v[18:33], v[114:117], v[144:147], v[18:33]
	ds_read_b128 v[140:143], v159 offset:34912
	ds_read_b128 v[144:147], v159 offset:43616
	s_waitcnt lgkmcnt(3)
	v_mfma_f32_32x32x16_f16 v[50:65], v[242:245], v[110:113], v[50:65]
	s_waitcnt lgkmcnt(2)
	v_mfma_f32_32x32x16_f16 v[34:49], v[246:249], v[110:113], v[34:49]
	v_mfma_f32_32x32x16_f16 v[2:17], v[106:109], v[242:245], v[2:17]
	v_mfma_f32_32x32x16_f16 v[18:33], v[106:109], v[246:249], v[18:33]
	ds_read_b128 v[242:245], v159 offset:34944
	ds_read_b128 v[246:249], v159 offset:43648
	s_waitcnt lgkmcnt(3)
	v_mfma_f32_32x32x16_f16 v[50:65], v[140:143], v[102:105], v[50:65]
	s_waitcnt lgkmcnt(2)
	v_mfma_f32_32x32x16_f16 v[34:49], v[144:147], v[102:105], v[34:49]
	v_mfma_f32_32x32x16_f16 v[2:17], v[98:101], v[140:143], v[2:17]
	v_mfma_f32_32x32x16_f16 v[18:33], v[98:101], v[144:147], v[18:33]
	ds_read_b128 v[186:189], v159 offset:34976
	ds_read_b128 v[206:209], v159 offset:43680
	s_waitcnt lgkmcnt(3)
	v_mfma_f32_32x32x16_f16 v[50:65], v[242:245], v[94:97], v[50:65]
	s_waitcnt lgkmcnt(2)
	v_mfma_f32_32x32x16_f16 v[34:49], v[246:249], v[94:97], v[34:49]
	v_mfma_f32_32x32x16_f16 v[2:17], v[86:89], v[242:245], v[2:17]
	v_mfma_f32_32x32x16_f16 v[18:33], v[86:89], v[246:249], v[18:33]
	ds_read_b128 v[140:143], v159 offset:35008
	ds_read_b128 v[144:147], v159 offset:43712
	s_waitcnt lgkmcnt(3)
	v_mfma_f32_32x32x16_f16 v[50:65], v[186:189], v[90:93], v[50:65]
	s_waitcnt lgkmcnt(2)
	v_mfma_f32_32x32x16_f16 v[34:49], v[206:209], v[90:93], v[34:49]
	v_mfma_f32_32x32x16_f16 v[2:17], v[78:81], v[186:189], v[2:17]
	v_mfma_f32_32x32x16_f16 v[18:33], v[78:81], v[206:209], v[18:33]
	ds_read_b128 v[186:189], v159 offset:35040
	ds_read_b128 v[206:209], v159 offset:43744
	s_waitcnt lgkmcnt(3)
	v_mfma_f32_32x32x16_f16 v[50:65], v[140:143], v[82:85], v[50:65]
	s_waitcnt lgkmcnt(2)
	v_mfma_f32_32x32x16_f16 v[34:49], v[144:147], v[82:85], v[34:49]
	v_mfma_f32_32x32x16_f16 v[2:17], v[70:73], v[140:143], v[2:17]
	v_lshlrev_b32_e32 v140, 3, v148
	v_and_b32_e32 v199, 0x1f8, v140
	global_load_dwordx2 v[148:149], v199, s[0:1]
	global_load_dwordx2 v[142:143], v199, s[0:1] offset:1024
	global_load_dwordx2 v[140:141], v199, s[0:1] offset:1536
	v_mfma_f32_32x32x16_f16 v[18:33], v[70:73], v[144:147], v[18:33]
	global_load_dwordx2 v[144:145], v199, s[0:1] offset:512
	global_load_dwordx2 v[146:147], v199, s[0:1] offset:2048
	s_waitcnt lgkmcnt(1)
	v_mfma_f32_32x32x16_f16 v[50:65], v[186:189], v[74:77], v[50:65]
	v_mfma_f32_32x32x16_f16 v[2:17], v[66:69], v[186:189], v[2:17]
	s_nop 10
	v_cvt_pk_f16_f32 v57, v56, v57
	v_cvt_pk_f16_f32 v56, v54, v55
	v_cvt_pk_f16_f32 v54, v50, v51
	s_waitcnt vmcnt(12)
	v_cvt_pk_f16_f32 v55, v52, v53
	s_waitcnt vmcnt(8)
	v_perm_b32 v50, v240, v138, s42
	v_perm_b32 v51, v240, v138, s43
	v_perm_b32 v52, v240, v139, s42
	v_perm_b32 v53, v240, v139, s43
	v_perm_b32 v139, v240, v136, s43
	v_pk_add_f16 v50, v50, s5 op_sel_hi:[1,0]
	v_pk_add_f16 v51, v51, s5 op_sel_hi:[1,0]
	v_pk_add_f16 v52, v52, s5 op_sel_hi:[1,0]
	v_pk_add_f16 v53, v53, s5 op_sel_hi:[1,0]
	v_perm_b32 v190, v240, v137, s42
	s_waitcnt lgkmcnt(0)
	v_mfma_f32_32x32x16_f16 v[18:33], v[66:69], v[206:209], v[18:33]
	v_perm_b32 v138, v240, v136, s42
	v_perm_b32 v191, v240, v137, s43
	v_pk_add_f16 v136, v138, s5 op_sel_hi:[1,0]
	v_pk_add_f16 v137, v139, s5 op_sel_hi:[1,0]
	v_pk_add_f16 v138, v190, s5 op_sel_hi:[1,0]
	v_pk_add_f16 v139, v191, s5 op_sel_hi:[1,0]
	v_cvt_pk_f16_f32 v65, v64, v65
	v_cvt_pk_f16_f32 v64, v62, v63
	v_cvt_pk_f16_f32 v63, v60, v61
	v_cvt_pk_f16_f32 v62, v58, v59
	v_mfma_f32_32x32x16_f16 v[34:49], v[206:209], v[74:77], v[34:49]
	v_mfma_f32_32x32x16_f16 v[2:17], v[54:57], v[50:53], v[2:17]
	s_waitcnt vmcnt(7)
	v_perm_b32 v58, v240, v134, s42
	v_perm_b32 v59, v240, v134, s43
	v_perm_b32 v60, v240, v135, s42
	v_perm_b32 v61, v240, v135, s43
	v_pk_add_f16 v58, v58, s5 op_sel_hi:[1,0]
	v_pk_add_f16 v59, v59, s5 op_sel_hi:[1,0]
	v_pk_add_f16 v60, v60, s5 op_sel_hi:[1,0]
	v_pk_add_f16 v61, v61, s5 op_sel_hi:[1,0]
	v_mfma_f32_32x32x16_f16 v[18:33], v[54:57], v[136:139], v[18:33]
	v_perm_b32 v134, v240, v154, s42
	v_perm_b32 v135, v240, v154, s43
	v_perm_b32 v154, v240, v155, s42
	v_perm_b32 v155, v240, v155, s43
	v_pk_add_f16 v210, v134, s5 op_sel_hi:[1,0]
	v_pk_add_f16 v211, v135, s5 op_sel_hi:[1,0]
	v_pk_add_f16 v212, v154, s5 op_sel_hi:[1,0]
	v_pk_add_f16 v213, v155, s5 op_sel_hi:[1,0]
	v_cvt_pk_f16_f32 v41, v40, v41
	v_cvt_pk_f16_f32 v40, v38, v39
	v_cvt_pk_f16_f32 v39, v36, v37
	v_cvt_pk_f16_f32 v38, v34, v35
	v_mfma_f32_32x32x16_f16 v[2:17], v[62:65], v[58:61], v[2:17]
	v_perm_b32 v34, v240, v132, s42
	v_perm_b32 v35, v240, v132, s43
	v_perm_b32 v36, v240, v133, s42
	v_perm_b32 v37, v240, v133, s43
	v_pk_add_f16 v34, v34, s5 op_sel_hi:[1,0]
	v_pk_add_f16 v35, v35, s5 op_sel_hi:[1,0]
	v_pk_add_f16 v36, v36, s5 op_sel_hi:[1,0]
	v_pk_add_f16 v37, v37, s5 op_sel_hi:[1,0]
	s_waitcnt vmcnt(6)
	v_mfma_f32_32x32x16_f16 v[18:33], v[62:65], v[210:213], v[18:33]
	v_perm_b32 v132, v240, v152, s42
	v_perm_b32 v133, v240, v152, s43
	v_perm_b32 v134, v240, v153, s42
	v_perm_b32 v53, v240, v153, s43
	v_pk_add_f16 v50, v132, s5 op_sel_hi:[1,0]
	v_pk_add_f16 v51, v133, s5 op_sel_hi:[1,0]
	v_pk_add_f16 v52, v134, s5 op_sel_hi:[1,0]
	v_pk_add_f16 v53, v53, s5 op_sel_hi:[1,0]
	v_cvt_pk_f16_f32 v49, v48, v49
	v_cvt_pk_f16_f32 v48, v46, v47
	v_cvt_pk_f16_f32 v47, v44, v45
	v_cvt_pk_f16_f32 v46, v42, v43
	v_mfma_f32_32x32x16_f16 v[2:17], v[38:41], v[34:37], v[2:17]
	v_perm_b32 v42, v240, v130, s42
	v_perm_b32 v43, v240, v130, s43
	v_perm_b32 v44, v240, v131, s42
	v_perm_b32 v45, v240, v131, s43
	v_pk_add_f16 v42, v42, s5 op_sel_hi:[1,0]
	v_pk_add_f16 v43, v43, s5 op_sel_hi:[1,0]
	v_pk_add_f16 v44, v44, s5 op_sel_hi:[1,0]
	v_pk_add_f16 v45, v45, s5 op_sel_hi:[1,0]
	s_waitcnt vmcnt(5)
	v_mfma_f32_32x32x16_f16 v[18:33], v[38:41], v[50:53], v[18:33]
	v_perm_b32 v34, v240, v150, s42
	v_perm_b32 v35, v240, v150, s43
	v_perm_b32 v36, v240, v151, s42
	v_perm_b32 v37, v240, v151, s43
	v_pk_add_f16 v34, v34, s5 op_sel_hi:[1,0]
	v_pk_add_f16 v35, v35, s5 op_sel_hi:[1,0]
	v_pk_add_f16 v36, v36, s5 op_sel_hi:[1,0]
	v_pk_add_f16 v37, v37, s5 op_sel_hi:[1,0]
	v_mfma_f32_32x32x16_f16 v[2:17], v[46:49], v[42:45], v[2:17]
	global_load_dwordx2 v[154:155], v199, s[0:1] offset:2560
	global_load_dwordx2 v[152:153], v199, s[0:1] offset:3072
	global_load_dwordx2 v[150:151], v199, s[0:1] offset:3584
	s_or_b32 s0, s8, 6
	s_ashr_i32 s1, s0, 31
	s_lshl_b64 s[0:1], s[0:1], 12
	s_add_u32 s0, s2, s0
	v_mfma_f32_32x32x16_f16 v[18:33], v[46:49], v[34:37], v[18:33]
	s_nop 7
	s_nop 4
	v_cvt_pk_f16_f32 v254, v2, v3
	v_cvt_pk_f16_f32 v255, v4, v5
	ds_write_b64 v251, v[254:255] offset:18432
	v_pk_add_f32 v[222:223], v[222:223], v[2:3]
	v_pk_fma_f32 v[194:195], v[2:3], v[2:3], v[194:195]
	v_pk_add_f32 v[220:221], v[220:221], v[4:5]
	v_pk_fma_f32 v[192:193], v[4:5], v[4:5], v[192:193]
	v_cvt_pk_f16_f32 v252, v6, v7
	v_cvt_pk_f16_f32 v253, v8, v9
	ds_write_b64 v251, v[252:253] offset:18448
	v_pk_add_f32 v[218:219], v[218:219], v[6:7]
	v_pk_fma_f32 v[184:185], v[6:7], v[6:7], v[184:185]
	v_pk_add_f32 v[216:217], v[216:217], v[8:9]
	v_pk_fma_f32 v[166:167], v[8:9], v[8:9], v[166:167]
	v_cvt_pk_f16_f32 v254, v10, v11
	v_cvt_pk_f16_f32 v255, v12, v13
	ds_write_b64 v251, v[254:255] offset:18464
	v_pk_add_f32 v[214:215], v[214:215], v[10:11]
	v_pk_fma_f32 v[164:165], v[10:11], v[10:11], v[164:165]
	v_pk_add_f32 v[204:205], v[204:205], v[12:13]
	v_pk_fma_f32 v[162:163], v[12:13], v[12:13], v[162:163]
	v_cvt_pk_f16_f32 v252, v14, v15
	v_cvt_pk_f16_f32 v253, v16, v17
	ds_write_b64 v251, v[252:253] offset:18480
	v_pk_add_f32 v[202:203], v[202:203], v[14:15]
	v_pk_fma_f32 v[160:161], v[14:15], v[14:15], v[160:161]
	v_pk_add_f32 v[196:197], v[196:197], v[16:17]
	v_pk_fma_f32 v[156:157], v[16:17], v[16:17], v[156:157]
	v_cvt_pk_f16_f32 v254, v18, v19
	v_cvt_pk_f16_f32 v255, v20, v21
	ds_write_b64 v251, v[254:255] offset:23040
	v_pk_add_f32 v[222:223], v[222:223], v[18:19]
	v_pk_fma_f32 v[194:195], v[18:19], v[18:19], v[194:195]
	v_pk_add_f32 v[220:221], v[220:221], v[20:21]
	v_pk_fma_f32 v[192:193], v[20:21], v[20:21], v[192:193]
	v_cvt_pk_f16_f32 v252, v22, v23
	v_cvt_pk_f16_f32 v253, v24, v25
	ds_write_b64 v251, v[252:253] offset:23056
	v_pk_add_f32 v[218:219], v[218:219], v[22:23]
	v_pk_fma_f32 v[184:185], v[22:23], v[22:23], v[184:185]
	v_pk_add_f32 v[216:217], v[216:217], v[24:25]
	v_pk_fma_f32 v[166:167], v[24:25], v[24:25], v[166:167]
	v_cvt_pk_f16_f32 v254, v26, v27
	v_cvt_pk_f16_f32 v255, v28, v29
	ds_write_b64 v251, v[254:255] offset:23072
	v_pk_add_f32 v[214:215], v[214:215], v[26:27]
	v_pk_fma_f32 v[164:165], v[26:27], v[26:27], v[164:165]
	v_pk_add_f32 v[204:205], v[204:205], v[28:29]
	v_pk_fma_f32 v[162:163], v[28:29], v[28:29], v[162:163]
	v_cvt_pk_f16_f32 v252, v30, v31
	v_cvt_pk_f16_f32 v253, v32, v33
	ds_write_b64 v251, v[252:253] offset:23088
	v_pk_add_f32 v[202:203], v[202:203], v[30:31]
	v_pk_fma_f32 v[160:161], v[30:31], v[30:31], v[160:161]
	v_pk_add_f32 v[196:197], v[196:197], v[32:33]
	v_pk_fma_f32 v[156:157], v[32:33], v[32:33], v[156:157]
	s_nop 3
	s_nop 0
	s_nop 0
	s_waitcnt lgkmcnt(0)
	s_barrier
	ds_read_b128 v[2:5], v159
	s_nop 2
	ds_read_b128 v[18:21], v159 offset:8704
	s_waitcnt lgkmcnt(1)
	v_mfma_f32_32x32x16_f16 v[50:65], v[2:5], v[126:129], 0
	v_lshlrev_b32_e32 v0, 3, v0
	s_addc_u32 s1, s3, s1
	v_and_b32_e32 v0, 0x1f8, v0
	global_load_dwordx2 v[138:139], v0, s[0:1]
	s_waitcnt lgkmcnt(0)
	v_mfma_f32_32x32x16_f16 v[34:49], v[18:21], v[126:129], 0
	v_mfma_f32_32x32x16_f16 v[2:17], v[122:125], v[2:5], v[168:183]
	v_mfma_f32_32x32x16_f16 v[18:33], v[122:125], v[18:21], v[168:183]
	ds_read_b128 v[130:133], v159 offset:32
	ds_read_b128 v[134:137], v159 offset:8736
	s_waitcnt lgkmcnt(1)
	v_mfma_f32_32x32x16_f16 v[50:65], v[130:133], v[118:121], v[50:65]
	s_waitcnt lgkmcnt(0)
	v_mfma_f32_32x32x16_f16 v[34:49], v[134:137], v[118:121], v[34:49]
	v_mfma_f32_32x32x16_f16 v[2:17], v[114:117], v[130:133], v[2:17]
	v_mfma_f32_32x32x16_f16 v[18:33], v[114:117], v[134:137], v[18:33]
	ds_read_b128 v[224:227], v159 offset:64
	ds_read_b128 v[228:231], v159 offset:8768
	ds_read_b128 v[130:133], v159 offset:96
	ds_read_b128 v[134:137], v159 offset:8800
	s_waitcnt lgkmcnt(3)
	v_mfma_f32_32x32x16_f16 v[50:65], v[224:227], v[110:113], v[50:65]
	s_waitcnt lgkmcnt(2)
	v_mfma_f32_32x32x16_f16 v[34:49], v[228:231], v[110:113], v[34:49]
	v_mfma_f32_32x32x16_f16 v[2:17], v[106:109], v[224:227], v[2:17]
	v_mfma_f32_32x32x16_f16 v[18:33], v[106:109], v[228:231], v[18:33]
	ds_read_b128 v[224:227], v159 offset:128
	ds_read_b128 v[228:231], v159 offset:8832
	s_waitcnt lgkmcnt(3)
	v_mfma_f32_32x32x16_f16 v[50:65], v[130:133], v[102:105], v[50:65]
	s_waitcnt lgkmcnt(2)
	v_mfma_f32_32x32x16_f16 v[34:49], v[134:137], v[102:105], v[34:49]
	v_mfma_f32_32x32x16_f16 v[2:17], v[98:101], v[130:133], v[2:17]
	v_mfma_f32_32x32x16_f16 v[18:33], v[98:101], v[134:137], v[18:33]
	ds_read_b128 v[130:133], v159 offset:160
	ds_read_b128 v[134:137], v159 offset:8864
	s_waitcnt lgkmcnt(3)
	v_mfma_f32_32x32x16_f16 v[50:65], v[224:227], v[94:97], v[50:65]
	s_waitcnt lgkmcnt(2)
	v_mfma_f32_32x32x16_f16 v[34:49], v[228:231], v[94:97], v[34:49]
	v_mfma_f32_32x32x16_f16 v[2:17], v[86:89], v[224:227], v[2:17]
	v_mfma_f32_32x32x16_f16 v[18:33], v[86:89], v[228:231], v[18:33]
	ds_read_b128 v[224:227], v159 offset:192
	ds_read_b128 v[228:231], v159 offset:8896
	s_waitcnt lgkmcnt(3)
	v_mfma_f32_32x32x16_f16 v[50:65], v[130:133], v[90:93], v[50:65]
	s_waitcnt lgkmcnt(2)
	v_mfma_f32_32x32x16_f16 v[34:49], v[134:137], v[90:93], v[34:49]
	v_mfma_f32_32x32x16_f16 v[2:17], v[78:81], v[130:133], v[2:17]
	v_mfma_f32_32x32x16_f16 v[18:33], v[78:81], v[134:137], v[18:33]
	ds_read_b128 v[232:235], v159 offset:224
	ds_read_b128 v[236:239], v159 offset:8928
	s_waitcnt lgkmcnt(3)
	v_mfma_f32_32x32x16_f16 v[50:65], v[224:227], v[82:85], v[50:65]
	global_load_dwordx2 v[134:135], v0, s[0:1] offset:512
	global_load_dwordx2 v[132:133], v0, s[0:1] offset:1024
	global_load_dwordx2 v[130:131], v0, s[0:1] offset:1536
	s_waitcnt lgkmcnt(2)
	v_mfma_f32_32x32x16_f16 v[34:49], v[228:231], v[82:85], v[34:49]
	global_load_dwordx2 v[136:137], v0, s[0:1] offset:2048
	v_mfma_f32_32x32x16_f16 v[2:17], v[70:73], v[224:227], v[2:17]
	v_mfma_f32_32x32x16_f16 v[18:33], v[70:73], v[228:231], v[18:33]
	s_waitcnt lgkmcnt(1)
	v_mfma_f32_32x32x16_f16 v[50:65], v[232:235], v[74:77], v[50:65]
	v_mfma_f32_32x32x16_f16 v[2:17], v[66:69], v[232:235], v[2:17]
	s_nop 10
	v_cvt_pk_f16_f32 v57, v56, v57
	v_cvt_pk_f16_f32 v56, v54, v55
	v_cvt_pk_f16_f32 v54, v50, v51
	s_waitcnt vmcnt(12)
	v_lshlrev_b32_e32 v50, 8, v148
	v_cvt_pk_f16_f32 v55, v52, v53
	v_perm_b32 v50, v50, v148, s4
	v_lshrrev_b32_e32 v51, 16, v148
	v_lshrrev_b32_e32 v52, 8, v148
	v_lshrrev_b32_e32 v53, 16, v149
	v_lshrrev_b32_e32 v148, 8, v149
	v_perm_b32 v51, v52, v51, s4
	v_lshlrev_b32_e32 v52, 8, v149
	v_perm_b32 v53, v148, v53, s4
	s_waitcnt vmcnt(8)
	v_perm_b32 v52, v52, v149, s4
	v_perm_b32 v149, v240, v146, s43
	v_perm_b32 v198, v240, v147, s42
	s_waitcnt lgkmcnt(0)
	v_mfma_f32_32x32x16_f16 v[18:33], v[66:69], v[236:239], v[18:33]
	v_or_b32_e32 v50, 0x64006400, v50
	v_or_b32_e32 v51, 0x64006400, v51
	v_or_b32_e32 v52, 0x64006400, v52
	v_or_b32_e32 v53, 0x64006400, v53
	v_pk_add_f16 v50, v50, s5 op_sel_hi:[1,0]
	v_pk_add_f16 v51, v51, s5 op_sel_hi:[1,0]
	v_pk_add_f16 v52, v52, s5 op_sel_hi:[1,0]
	v_pk_add_f16 v53, v53, s5 op_sel_hi:[1,0]
	v_perm_b32 v148, v240, v146, s42
	v_perm_b32 v200, v240, v147, s43
	v_pk_add_f16 v146, v148, s5 op_sel_hi:[1,0]
	v_pk_add_f16 v147, v149, s5 op_sel_hi:[1,0]
	v_pk_add_f16 v148, v198, s5 op_sel_hi:[1,0]
	v_pk_add_f16 v149, v200, s5 op_sel_hi:[1,0]
	v_cvt_pk_f16_f32 v65, v64, v65
	v_cvt_pk_f16_f32 v64, v62, v63
	v_cvt_pk_f16_f32 v62, v58, v59
	v_cvt_pk_f16_f32 v63, v60, v61
	s_waitcnt vmcnt(7)
	v_mfma_f32_32x32x16_f16 v[34:49], v[236:239], v[74:77], v[34:49]
	v_mfma_f32_32x32x16_f16 v[2:17], v[54:57], v[50:53], v[2:17]
	v_perm_b32 v58, v240, v144, s42
	v_perm_b32 v59, v240, v144, s43
	v_perm_b32 v60, v240, v145, s42
	v_perm_b32 v61, v240, v145, s43
	v_mfma_f32_32x32x16_f16 v[18:33], v[54:57], v[146:149], v[18:33]
	v_pk_add_f16 v58, v58, s5 op_sel_hi:[1,0]
	v_pk_add_f16 v59, v59, s5 op_sel_hi:[1,0]
	v_pk_add_f16 v60, v60, s5 op_sel_hi:[1,0]
	v_pk_add_f16 v61, v61, s5 op_sel_hi:[1,0]
	v_perm_b32 v144, v240, v154, s42
	v_perm_b32 v145, v240, v154, s43
	v_perm_b32 v154, v240, v155, s42
	v_perm_b32 v155, v240, v155, s43
	v_pk_add_f16 v224, v144, s5 op_sel_hi:[1,0]
	v_pk_add_f16 v225, v145, s5 op_sel_hi:[1,0]
	v_pk_add_f16 v226, v154, s5 op_sel_hi:[1,0]
	v_pk_add_f16 v227, v155, s5 op_sel_hi:[1,0]
	v_cvt_pk_f16_f32 v41, v40, v41
	v_cvt_pk_f16_f32 v40, v38, v39
	v_cvt_pk_f16_f32 v39, v36, v37
	v_cvt_pk_f16_f32 v38, v34, v35
	s_waitcnt vmcnt(6)
	v_mfma_f32_32x32x16_f16 v[2:17], v[62:65], v[58:61], v[2:17]
	v_perm_b32 v34, v240, v142, s42
	v_perm_b32 v35, v240, v142, s43
	v_mfma_f32_32x32x16_f16 v[18:33], v[62:65], v[224:227], v[18:33]
	v_perm_b32 v36, v240, v143, s42
	v_perm_b32 v37, v240, v143, s43
	v_pk_add_f16 v34, v34, s5 op_sel_hi:[1,0]
	v_pk_add_f16 v35, v35, s5 op_sel_hi:[1,0]
	v_pk_add_f16 v36, v36, s5 op_sel_hi:[1,0]
	v_pk_add_f16 v37, v37, s5 op_sel_hi:[1,0]
	v_perm_b32 v142, v240, v152, s42
	v_perm_b32 v143, v240, v152, s43
	v_perm_b32 v144, v240, v153, s42
	v_perm_b32 v53, v240, v153, s43
	v_pk_add_f16 v50, v142, s5 op_sel_hi:[1,0]
	v_pk_add_f16 v51, v143, s5 op_sel_hi:[1,0]
	v_pk_add_f16 v52, v144, s5 op_sel_hi:[1,0]
	v_pk_add_f16 v53, v53, s5 op_sel_hi:[1,0]
	v_cvt_pk_f16_f32 v49, v48, v49
	v_cvt_pk_f16_f32 v48, v46, v47
	v_cvt_pk_f16_f32 v47, v44, v45
	v_cvt_pk_f16_f32 v46, v42, v43
	v_mfma_f32_32x32x16_f16 v[2:17], v[38:41], v[34:37], v[2:17]
	s_waitcnt vmcnt(5)
	v_mfma_f32_32x32x16_f16 v[18:33], v[38:41], v[50:53], v[18:33]
	v_perm_b32 v42, v240, v140, s42
	v_perm_b32 v43, v240, v140, s43
	v_perm_b32 v44, v240, v141, s42
	v_perm_b32 v45, v240, v141, s43
	v_perm_b32 v34, v240, v150, s42
	v_perm_b32 v35, v240, v150, s43
	v_perm_b32 v36, v240, v151, s42
	v_perm_b32 v37, v240, v151, s43
	v_pk_add_f16 v42, v42, s5 op_sel_hi:[1,0]
	v_pk_add_f16 v43, v43, s5 op_sel_hi:[1,0]
	v_pk_add_f16 v44, v44, s5 op_sel_hi:[1,0]
	v_pk_add_f16 v45, v45, s5 op_sel_hi:[1,0]
	v_pk_add_f16 v34, v34, s5 op_sel_hi:[1,0]
	v_pk_add_f16 v35, v35, s5 op_sel_hi:[1,0]
	v_pk_add_f16 v36, v36, s5 op_sel_hi:[1,0]
	v_pk_add_f16 v37, v37, s5 op_sel_hi:[1,0]
	v_mfma_f32_32x32x16_f16 v[2:17], v[46:49], v[42:45], v[2:17]
	global_load_dwordx2 v[142:143], v0, s[0:1] offset:2560
	global_load_dwordx2 v[140:141], v0, s[0:1] offset:3072
	global_load_dwordx2 v[64:65], v0, s[0:1] offset:3584
	v_mfma_f32_32x32x16_f16 v[18:33], v[46:49], v[34:37], v[18:33]
	s_nop 7
	s_nop 4
	v_cvt_pk_f16_f32 v254, v2, v3
	v_cvt_pk_f16_f32 v255, v4, v5
	ds_write_b64 v251, v[254:255] offset:0
	v_pk_add_f32 v[222:223], v[222:223], v[2:3]
	v_pk_fma_f32 v[194:195], v[2:3], v[2:3], v[194:195]
	v_pk_add_f32 v[220:221], v[220:221], v[4:5]
	v_pk_fma_f32 v[192:193], v[4:5], v[4:5], v[192:193]
	v_cvt_pk_f16_f32 v252, v6, v7
	v_cvt_pk_f16_f32 v253, v8, v9
	ds_write_b64 v251, v[252:253] offset:16
	v_pk_add_f32 v[218:219], v[218:219], v[6:7]
	v_pk_fma_f32 v[184:185], v[6:7], v[6:7], v[184:185]
	v_pk_add_f32 v[216:217], v[216:217], v[8:9]
	v_pk_fma_f32 v[166:167], v[8:9], v[8:9], v[166:167]
	v_cvt_pk_f16_f32 v254, v10, v11
	v_cvt_pk_f16_f32 v255, v12, v13
	ds_write_b64 v251, v[254:255] offset:32
	v_pk_add_f32 v[214:215], v[214:215], v[10:11]
	v_pk_fma_f32 v[164:165], v[10:11], v[10:11], v[164:165]
	v_pk_add_f32 v[204:205], v[204:205], v[12:13]
	v_pk_fma_f32 v[162:163], v[12:13], v[12:13], v[162:163]
	v_cvt_pk_f16_f32 v252, v14, v15
	v_cvt_pk_f16_f32 v253, v16, v17
	ds_write_b64 v251, v[252:253] offset:48
	v_pk_add_f32 v[202:203], v[202:203], v[14:15]
	v_pk_fma_f32 v[160:161], v[14:15], v[14:15], v[160:161]
	v_pk_add_f32 v[196:197], v[196:197], v[16:17]
	v_pk_fma_f32 v[156:157], v[16:17], v[16:17], v[156:157]
	v_cvt_pk_f16_f32 v254, v18, v19
	v_cvt_pk_f16_f32 v255, v20, v21
	ds_write_b64 v251, v[254:255] offset:4608
	v_pk_add_f32 v[222:223], v[222:223], v[18:19]
	v_pk_fma_f32 v[194:195], v[18:19], v[18:19], v[194:195]
	v_pk_add_f32 v[220:221], v[220:221], v[20:21]
	v_pk_fma_f32 v[192:193], v[20:21], v[20:21], v[192:193]
	v_cvt_pk_f16_f32 v252, v22, v23
	v_cvt_pk_f16_f32 v253, v24, v25
	ds_write_b64 v251, v[252:253] offset:4624
	v_pk_add_f32 v[218:219], v[218:219], v[22:23]
	v_pk_fma_f32 v[184:185], v[22:23], v[22:23], v[184:185]
	v_pk_add_f32 v[216:217], v[216:217], v[24:25]
	v_pk_fma_f32 v[166:167], v[24:25], v[24:25], v[166:167]
	v_cvt_pk_f16_f32 v254, v26, v27
	v_cvt_pk_f16_f32 v255, v28, v29
	ds_write_b64 v251, v[254:255] offset:4640
	v_pk_add_f32 v[214:215], v[214:215], v[26:27]
	v_pk_fma_f32 v[164:165], v[26:27], v[26:27], v[164:165]
	v_pk_add_f32 v[204:205], v[204:205], v[28:29]
	v_pk_fma_f32 v[162:163], v[28:29], v[28:29], v[162:163]
	v_cvt_pk_f16_f32 v252, v30, v31
	v_cvt_pk_f16_f32 v253, v32, v33
	ds_write_b64 v251, v[252:253] offset:4656
	v_pk_add_f32 v[202:203], v[202:203], v[30:31]
	v_pk_fma_f32 v[160:161], v[30:31], v[30:31], v[160:161]
	v_pk_add_f32 v[196:197], v[196:197], v[32:33]
	v_pk_fma_f32 v[156:157], v[32:33], v[32:33], v[156:157]
	s_nop 7
	s_waitcnt lgkmcnt(0)
	s_barrier
	s_nop 1
	ds_read_b128 v[16:19], v159 offset:43520
	s_waitcnt lgkmcnt(0)
	v_mfma_f32_32x32x16_f16 v[32:47], v[16:19], v[126:129], 0
	ds_read_b128 v[2:5], v159 offset:34816
	s_waitcnt lgkmcnt(0)
	v_mfma_f32_32x32x16_f16 v[48:63], v[2:5], v[126:129], 0
	ds_read_b128 v[126:129], v159 offset:34848
	s_waitcnt lgkmcnt(0)
	v_mfma_f32_32x32x16_f16 v[48:63], v[126:129], v[118:121], v[48:63]
	v_mfma_f32_32x32x16_f16 v[0:15], v[122:125], v[2:5], v[168:183]
	v_mfma_f32_32x32x16_f16 v[0:15], v[114:117], v[126:129], v[0:15]
	v_mfma_f32_32x32x16_f16 v[16:31], v[122:125], v[16:19], v[168:183]
	ds_read_b128 v[122:125], v159 offset:43552
	s_waitcnt lgkmcnt(0)
	v_mfma_f32_32x32x16_f16 v[32:47], v[122:125], v[118:121], v[32:47]
	v_mfma_f32_32x32x16_f16 v[16:31], v[114:117], v[122:125], v[16:31]
	ds_read_b128 v[118:121], v159 offset:34880
	ds_read_b128 v[114:117], v159 offset:43584
	s_waitcnt lgkmcnt(1)
	v_mfma_f32_32x32x16_f16 v[48:63], v[118:121], v[110:113], v[48:63]
	s_waitcnt lgkmcnt(0)
	v_mfma_f32_32x32x16_f16 v[32:47], v[114:117], v[110:113], v[32:47]
	v_mfma_f32_32x32x16_f16 v[0:15], v[106:109], v[118:121], v[0:15]
	ds_read_b128 v[110:113], v159 offset:34912
	v_mfma_f32_32x32x16_f16 v[16:31], v[106:109], v[114:117], v[16:31]
	ds_read_b128 v[106:109], v159 offset:43616
	s_waitcnt lgkmcnt(1)
	v_mfma_f32_32x32x16_f16 v[48:63], v[110:113], v[102:105], v[48:63]
	s_waitcnt lgkmcnt(0)
	v_mfma_f32_32x32x16_f16 v[32:47], v[106:109], v[102:105], v[32:47]
	v_mfma_f32_32x32x16_f16 v[0:15], v[98:101], v[110:113], v[0:15]
	ds_read_b128 v[102:105], v159 offset:34944
	v_mfma_f32_32x32x16_f16 v[16:31], v[98:101], v[106:109], v[16:31]
	ds_read_b128 v[98:101], v159 offset:43648
	s_waitcnt lgkmcnt(1)
	v_mfma_f32_32x32x16_f16 v[48:63], v[102:105], v[94:97], v[48:63]
	s_waitcnt lgkmcnt(0)
	v_mfma_f32_32x32x16_f16 v[32:47], v[98:101], v[94:97], v[32:47]
	v_mfma_f32_32x32x16_f16 v[0:15], v[86:89], v[102:105], v[0:15]
	ds_read_b128 v[94:97], v159 offset:34976
	v_mfma_f32_32x32x16_f16 v[16:31], v[86:89], v[98:101], v[16:31]
	ds_read_b128 v[86:89], v159 offset:43680
	s_waitcnt lgkmcnt(1)
	v_mfma_f32_32x32x16_f16 v[48:63], v[94:97], v[90:93], v[48:63]
	s_waitcnt lgkmcnt(0)
	v_mfma_f32_32x32x16_f16 v[32:47], v[86:89], v[90:93], v[32:47]
	v_mfma_f32_32x32x16_f16 v[0:15], v[78:81], v[94:97], v[0:15]
	ds_read_b128 v[90:93], v159 offset:35008
	v_mfma_f32_32x32x16_f16 v[16:31], v[78:81], v[86:89], v[16:31]
	ds_read_b128 v[78:81], v159 offset:43712
	s_waitcnt lgkmcnt(1)
	v_mfma_f32_32x32x16_f16 v[48:63], v[90:93], v[82:85], v[48:63]
	s_waitcnt lgkmcnt(0)
	v_mfma_f32_32x32x16_f16 v[32:47], v[78:81], v[82:85], v[32:47]
	v_mfma_f32_32x32x16_f16 v[0:15], v[70:73], v[90:93], v[0:15]
	ds_read_b128 v[82:85], v159 offset:35040
	v_mfma_f32_32x32x16_f16 v[16:31], v[70:73], v[78:81], v[16:31]
	ds_read_b128 v[70:73], v159 offset:43744
	s_waitcnt lgkmcnt(1)
	v_mfma_f32_32x32x16_f16 v[48:63], v[82:85], v[74:77], v[48:63]
	v_mfma_f32_32x32x16_f16 v[0:15], v[66:69], v[82:85], v[0:15]
	s_nop 3
	s_nop 6
	v_cvt_pk_f16_f32 v55, v54, v55
	v_cvt_pk_f16_f32 v54, v52, v53
	v_cvt_pk_f16_f32 v53, v50, v51
	v_cvt_pk_f16_f32 v52, v48, v49
	s_waitcnt vmcnt(3)
	s_waitcnt lgkmcnt(0)
	v_mfma_f32_32x32x16_f16 v[16:31], v[66:69], v[70:73], v[16:31]
	v_lshrrev_b32_e32 v69, 16, v139
	v_mfma_f32_32x32x16_f16 v[32:47], v[70:73], v[74:77], v[32:47]
	v_lshrrev_b32_e32 v70, 8, v139
	v_perm_b32 v69, v70, v69, s4
	v_perm_b32 v66, v240, v138, s42
	v_perm_b32 v67, v240, v138, s43
	v_perm_b32 v68, v240, v139, s42
	v_or_b32_e32 v69, 0x64006400, v69
	v_pk_add_f16 v66, v66, s5 op_sel_hi:[1,0]
	v_pk_add_f16 v67, v67, s5 op_sel_hi:[1,0]
	v_pk_add_f16 v68, v68, s5 op_sel_hi:[1,0]
	v_pk_add_f16 v69, v69, s5 op_sel_hi:[1,0]
	s_nop 1
	v_mfma_f32_32x32x16_f16 v[0:15], v[52:55], v[66:69], v[0:15]
	v_perm_b32 v48, v240, v136, s42
	v_perm_b32 v49, v240, v136, s43
	v_perm_b32 v50, v240, v137, s42
	v_perm_b32 v51, v240, v137, s43
	v_pk_add_f16 v48, v48, s5 op_sel_hi:[1,0]
	v_pk_add_f16 v49, v49, s5 op_sel_hi:[1,0]
	v_pk_add_f16 v50, v50, s5 op_sel_hi:[1,0]
	v_pk_add_f16 v51, v51, s5 op_sel_hi:[1,0]
	v_cvt_pk_f16_f32 v39, v38, v39
	v_cvt_pk_f16_f32 v38, v36, v37
	v_mfma_f32_32x32x16_f16 v[16:31], v[52:55], v[48:51], v[16:31]
	v_perm_b32 v48, v240, v134, s42
	v_perm_b32 v49, v240, v134, s43
	v_perm_b32 v50, v240, v135, s42
	v_perm_b32 v51, v240, v135, s43
	v_pk_add_f16 v48, v48, s5 op_sel_hi:[1,0]
	v_pk_add_f16 v49, v49, s5 op_sel_hi:[1,0]
	v_pk_add_f16 v50, v50, s5 op_sel_hi:[1,0]
	v_pk_add_f16 v51, v51, s5 op_sel_hi:[1,0]
	v_cvt_pk_f16_f32 v55, v62, v63
	v_cvt_pk_f16_f32 v54, v60, v61
	v_cvt_pk_f16_f32 v53, v58, v59
	v_cvt_pk_f16_f32 v52, v56, v57
	s_waitcnt vmcnt(2)
	v_cvt_pk_f16_f32 v37, v34, v35
	v_mfma_f32_32x32x16_f16 v[0:15], v[52:55], v[48:51], v[0:15]
	v_perm_b32 v48, v240, v142, s42
	v_perm_b32 v49, v240, v142, s43
	v_perm_b32 v50, v240, v143, s42
	v_perm_b32 v51, v240, v143, s43
	v_pk_add_f16 v48, v48, s5 op_sel_hi:[1,0]
	v_pk_add_f16 v49, v49, s5 op_sel_hi:[1,0]
	v_pk_add_f16 v50, v50, s5 op_sel_hi:[1,0]
	v_pk_add_f16 v51, v51, s5 op_sel_hi:[1,0]
	v_cvt_pk_f16_f32 v36, v32, v33
	s_waitcnt vmcnt(1)
	v_mfma_f32_32x32x16_f16 v[16:31], v[52:55], v[48:51], v[16:31]
	v_lshrrev_b32_e32 v51, 16, v133
	v_lshrrev_b32_e32 v52, 8, v133
	v_perm_b32 v51, v52, v51, s4
	v_perm_b32 v48, v240, v132, s42
	v_perm_b32 v49, v240, v132, s43
	v_perm_b32 v50, v240, v133, s42
	v_or_b32_e32 v51, 0x64006400, v51
	v_pk_add_f16 v48, v48, s5 op_sel_hi:[1,0]
	v_pk_add_f16 v49, v49, s5 op_sel_hi:[1,0]
	v_pk_add_f16 v50, v50, s5 op_sel_hi:[1,0]
	v_pk_add_f16 v51, v51, s5 op_sel_hi:[1,0]
	s_nop 1
	v_mfma_f32_32x32x16_f16 v[0:15], v[36:39], v[48:51], v[0:15]
	v_perm_b32 v32, v240, v140, s42
	v_perm_b32 v33, v240, v140, s43
	v_perm_b32 v34, v240, v141, s42
	v_perm_b32 v35, v240, v141, s43
	v_pk_add_f16 v32, v32, s5 op_sel_hi:[1,0]
	v_pk_add_f16 v33, v33, s5 op_sel_hi:[1,0]
	v_pk_add_f16 v34, v34, s5 op_sel_hi:[1,0]
	v_pk_add_f16 v35, v35, s5 op_sel_hi:[1,0]
	s_nop 1
	v_mfma_f32_32x32x16_f16 v[16:31], v[36:39], v[32:35], v[16:31]
	v_perm_b32 v32, v240, v130, s42
	v_perm_b32 v33, v240, v130, s43
	v_perm_b32 v34, v240, v131, s42
	v_perm_b32 v35, v240, v131, s43
	v_pk_add_f16 v32, v32, s5 op_sel_hi:[1,0]
	v_pk_add_f16 v33, v33, s5 op_sel_hi:[1,0]
	v_pk_add_f16 v34, v34, s5 op_sel_hi:[1,0]
	v_pk_add_f16 v35, v35, s5 op_sel_hi:[1,0]
	v_cvt_pk_f16_f32 v39, v46, v47
	v_cvt_pk_f16_f32 v38, v44, v45
	v_cvt_pk_f16_f32 v37, v42, v43
	v_cvt_pk_f16_f32 v36, v40, v41
	s_waitcnt vmcnt(0)
	s_nop 0
	v_mfma_f32_32x32x16_f16 v[0:15], v[36:39], v[32:35], v[0:15]
	v_perm_b32 v32, v240, v64, s42
	v_perm_b32 v33, v240, v64, s43
	v_perm_b32 v34, v240, v65, s42
	v_perm_b32 v35, v240, v65, s43
	v_pk_add_f16 v32, v32, s5 op_sel_hi:[1,0]
	v_pk_add_f16 v33, v33, s5 op_sel_hi:[1,0]
	v_pk_add_f16 v34, v34, s5 op_sel_hi:[1,0]
	v_pk_add_f16 v35, v35, s5 op_sel_hi:[1,0]
	s_nop 3
	v_mfma_f32_32x32x16_f16 v[16:31], v[36:39], v[32:35], v[16:31]
	s_nop 7
	s_nop 4
	v_cvt_pk_f16_f32 v254, v0, v1
	v_cvt_pk_f16_f32 v255, v2, v3
	ds_write_b64 v251, v[254:255] offset:18432
	v_pk_add_f32 v[222:223], v[222:223], v[0:1]
	v_pk_fma_f32 v[194:195], v[0:1], v[0:1], v[194:195]
	v_pk_add_f32 v[220:221], v[220:221], v[2:3]
	v_pk_fma_f32 v[192:193], v[2:3], v[2:3], v[192:193]
	v_cvt_pk_f16_f32 v252, v4, v5
	v_cvt_pk_f16_f32 v253, v6, v7
	ds_write_b64 v251, v[252:253] offset:18448
	v_pk_add_f32 v[218:219], v[218:219], v[4:5]
	v_pk_fma_f32 v[184:185], v[4:5], v[4:5], v[184:185]
	v_pk_add_f32 v[216:217], v[216:217], v[6:7]
	v_pk_fma_f32 v[166:167], v[6:7], v[6:7], v[166:167]
	v_cvt_pk_f16_f32 v254, v8, v9
	v_cvt_pk_f16_f32 v255, v10, v11
	ds_write_b64 v251, v[254:255] offset:18464
	v_pk_add_f32 v[214:215], v[214:215], v[8:9]
	v_pk_fma_f32 v[164:165], v[8:9], v[8:9], v[164:165]
	v_pk_add_f32 v[204:205], v[204:205], v[10:11]
	v_pk_fma_f32 v[162:163], v[10:11], v[10:11], v[162:163]
	v_cvt_pk_f16_f32 v252, v12, v13
	v_cvt_pk_f16_f32 v253, v14, v15
	ds_write_b64 v251, v[252:253] offset:18480
	v_pk_add_f32 v[202:203], v[202:203], v[12:13]
	v_pk_fma_f32 v[160:161], v[12:13], v[12:13], v[160:161]
	v_pk_add_f32 v[196:197], v[196:197], v[14:15]
	v_pk_fma_f32 v[156:157], v[14:15], v[14:15], v[156:157]
	v_cvt_pk_f16_f32 v254, v16, v17
	v_cvt_pk_f16_f32 v255, v18, v19
	ds_write_b64 v251, v[254:255] offset:23040
	v_pk_add_f32 v[222:223], v[222:223], v[16:17]
	v_pk_fma_f32 v[194:195], v[16:17], v[16:17], v[194:195]
	v_pk_add_f32 v[220:221], v[220:221], v[18:19]
	v_pk_fma_f32 v[192:193], v[18:19], v[18:19], v[192:193]
	v_cvt_pk_f16_f32 v252, v20, v21
	v_cvt_pk_f16_f32 v253, v22, v23
	ds_write_b64 v251, v[252:253] offset:23056
	v_pk_add_f32 v[218:219], v[218:219], v[20:21]
	v_pk_fma_f32 v[184:185], v[20:21], v[20:21], v[184:185]
	v_pk_add_f32 v[216:217], v[216:217], v[22:23]
	v_pk_fma_f32 v[166:167], v[22:23], v[22:23], v[166:167]
	v_cvt_pk_f16_f32 v254, v24, v25
	v_cvt_pk_f16_f32 v255, v26, v27
	ds_write_b64 v251, v[254:255] offset:23072
	v_pk_add_f32 v[214:215], v[214:215], v[24:25]
	v_pk_fma_f32 v[164:165], v[24:25], v[24:25], v[164:165]
	v_pk_add_f32 v[204:205], v[204:205], v[26:27]
	v_pk_fma_f32 v[162:163], v[26:27], v[26:27], v[162:163]
	v_cvt_pk_f16_f32 v252, v28, v29
	v_cvt_pk_f16_f32 v253, v30, v31
	ds_write_b64 v251, v[252:253] offset:23088
	v_pk_add_f32 v[202:203], v[202:203], v[28:29]
	v_pk_fma_f32 v[160:161], v[28:29], v[28:29], v[160:161]
	v_pk_add_f32 v[196:197], v[196:197], v[30:31]
	v_pk_fma_f32 v[156:157], v[30:31], v[30:31], v[156:157]
	s_nop 4
	s_nop 0
	v_add_f32_dpp v222, v222, v222 row_half_mirror row_mask:0xf bank_mask:0x5
	v_add_f32_dpp v222, v223, v223 row_half_mirror row_mask:0xf bank_mask:0xa
	v_add_f32_dpp v220, v220, v220 row_half_mirror row_mask:0xf bank_mask:0x5
	v_add_f32_dpp v220, v221, v221 row_half_mirror row_mask:0xf bank_mask:0xa
	v_add_f32_dpp v218, v218, v218 row_half_mirror row_mask:0xf bank_mask:0x5
	v_add_f32_dpp v218, v219, v219 row_half_mirror row_mask:0xf bank_mask:0xa
	v_add_f32_dpp v216, v216, v216 row_half_mirror row_mask:0xf bank_mask:0x5
	v_add_f32_dpp v216, v217, v217 row_half_mirror row_mask:0xf bank_mask:0xa
	v_add_f32_dpp v214, v214, v214 row_half_mirror row_mask:0xf bank_mask:0x5
	v_add_f32_dpp v214, v215, v215 row_half_mirror row_mask:0xf bank_mask:0xa
	v_add_f32_dpp v204, v204, v204 row_half_mirror row_mask:0xf bank_mask:0x5
	v_add_f32_dpp v204, v205, v205 row_half_mirror row_mask:0xf bank_mask:0xa
	v_add_f32_dpp v202, v202, v202 row_half_mirror row_mask:0xf bank_mask:0x5
	v_add_f32_dpp v202, v203, v203 row_half_mirror row_mask:0xf bank_mask:0xa
	v_add_f32_dpp v196, v196, v196 row_half_mirror row_mask:0xf bank_mask:0x5
	v_add_f32_dpp v196, v197, v197 row_half_mirror row_mask:0xf bank_mask:0xa
	v_add_f32_dpp v194, v194, v194 row_half_mirror row_mask:0xf bank_mask:0x5
	v_add_f32_dpp v194, v195, v195 row_half_mirror row_mask:0xf bank_mask:0xa
	v_add_f32_dpp v192, v192, v192 row_half_mirror row_mask:0xf bank_mask:0x5
	v_add_f32_dpp v192, v193, v193 row_half_mirror row_mask:0xf bank_mask:0xa
	v_add_f32_dpp v184, v184, v184 row_half_mirror row_mask:0xf bank_mask:0x5
	v_add_f32_dpp v184, v185, v185 row_half_mirror row_mask:0xf bank_mask:0xa
	v_add_f32_dpp v166, v166, v166 row_half_mirror row_mask:0xf bank_mask:0x5
	v_add_f32_dpp v166, v167, v167 row_half_mirror row_mask:0xf bank_mask:0xa
	v_add_f32_dpp v164, v164, v164 row_half_mirror row_mask:0xf bank_mask:0x5
	v_add_f32_dpp v164, v165, v165 row_half_mirror row_mask:0xf bank_mask:0xa
	v_add_f32_dpp v162, v162, v162 row_half_mirror row_mask:0xf bank_mask:0x5
	v_add_f32_dpp v162, v163, v163 row_half_mirror row_mask:0xf bank_mask:0xa
	v_add_f32_dpp v160, v160, v160 row_half_mirror row_mask:0xf bank_mask:0x5
	v_add_f32_dpp v160, v161, v161 row_half_mirror row_mask:0xf bank_mask:0xa
	v_add_f32_dpp v156, v156, v156 row_half_mirror row_mask:0xf bank_mask:0x5
	v_add_f32_dpp v156, v157, v157 row_half_mirror row_mask:0xf bank_mask:0xa
	v_add_f32_dpp v222, v222, v222 row_ror:8 row_mask:0xf bank_mask:0x3
	v_add_f32_dpp v222, v220, v220 row_ror:8 row_mask:0xf bank_mask:0xc
	v_add_f32_dpp v218, v218, v218 row_ror:8 row_mask:0xf bank_mask:0x3
	v_add_f32_dpp v218, v216, v216 row_ror:8 row_mask:0xf bank_mask:0xc
	v_add_f32_dpp v214, v214, v214 row_ror:8 row_mask:0xf bank_mask:0x3
	v_add_f32_dpp v214, v204, v204 row_ror:8 row_mask:0xf bank_mask:0xc
	v_add_f32_dpp v202, v202, v202 row_ror:8 row_mask:0xf bank_mask:0x3
	v_add_f32_dpp v202, v196, v196 row_ror:8 row_mask:0xf bank_mask:0xc
	v_add_f32_dpp v194, v194, v194 row_ror:8 row_mask:0xf bank_mask:0x3
	v_add_f32_dpp v194, v192, v192 row_ror:8 row_mask:0xf bank_mask:0xc
	v_add_f32_dpp v184, v184, v184 row_ror:8 row_mask:0xf bank_mask:0x3
	v_add_f32_dpp v184, v166, v166 row_ror:8 row_mask:0xf bank_mask:0xc
	v_add_f32_dpp v164, v164, v164 row_ror:8 row_mask:0xf bank_mask:0x3
	v_add_f32_dpp v164, v162, v162 row_ror:8 row_mask:0xf bank_mask:0xc
	v_add_f32_dpp v160, v160, v160 row_ror:8 row_mask:0xf bank_mask:0x3
	v_add_f32_dpp v160, v156, v156 row_ror:8 row_mask:0xf bank_mask:0xc
	v_add_f32_dpp v222, v222, v222 quad_perm:[1,0,3,2] row_mask:0xf bank_mask:0xf
	v_add_f32_dpp v218, v218, v218 quad_perm:[1,0,3,2] row_mask:0xf bank_mask:0xf
	v_add_f32_dpp v214, v214, v214 quad_perm:[1,0,3,2] row_mask:0xf bank_mask:0xf
	v_add_f32_dpp v202, v202, v202 quad_perm:[1,0,3,2] row_mask:0xf bank_mask:0xf
	v_add_f32_dpp v194, v194, v194 quad_perm:[1,0,3,2] row_mask:0xf bank_mask:0xf
	v_add_f32_dpp v184, v184, v184 quad_perm:[1,0,3,2] row_mask:0xf bank_mask:0xf
	v_add_f32_dpp v164, v164, v164 quad_perm:[1,0,3,2] row_mask:0xf bank_mask:0xf
	v_add_f32_dpp v160, v160, v160 quad_perm:[1,0,3,2] row_mask:0xf bank_mask:0xf
	v_add_f32_dpp v222, v222, v222 quad_perm:[2,3,0,1] row_mask:0xf bank_mask:0xf
	v_add_f32_dpp v218, v218, v218 quad_perm:[2,3,0,1] row_mask:0xf bank_mask:0xf
	v_add_f32_dpp v214, v214, v214 quad_perm:[2,3,0,1] row_mask:0xf bank_mask:0xf
	v_add_f32_dpp v202, v202, v202 quad_perm:[2,3,0,1] row_mask:0xf bank_mask:0xf
	v_add_f32_dpp v194, v194, v194 quad_perm:[2,3,0,1] row_mask:0xf bank_mask:0xf
	v_add_f32_dpp v184, v184, v184 quad_perm:[2,3,0,1] row_mask:0xf bank_mask:0xf
	v_add_f32_dpp v164, v164, v164 quad_perm:[2,3,0,1] row_mask:0xf bank_mask:0xf
	v_add_f32_dpp v160, v160, v160 quad_perm:[2,3,0,1] row_mask:0xf bank_mask:0xf
	s_mov_b32 exec_lo, 0x11111111
	s_mov_b32 exec_hi, 0x11111111
	ds_add_f32 v250, v222 offset:0
	ds_add_f32 v250, v218 offset:32
	ds_add_f32 v250, v214 offset:64
	ds_add_f32 v250, v202 offset:96
	ds_add_f32 v250, v194 offset:256
	ds_add_f32 v250, v184 offset:288
	ds_add_f32 v250, v164 offset:320
	ds_add_f32 v250, v160 offset:352
	s_mov_b64 exec, -1
	s_waitcnt lgkmcnt(0)
	s_barrier
	s_cmp_lg_u32 s50, 0
	s_cbranch_scc1 .LBB2_27
	v_mbcnt_lo_u32_b32 v2, -1, 0
	v_mbcnt_hi_u32_b32 v2, -1, v2
	v_and_b32_e32 v3, 32, v2
	v_add_u32_e32 v4, v2, v3
	v_lshl_add_u32 v5, v4, 2, s49
	ds_read_b32 v6, v5
	v_lshl_add_u32 v4, v3, 1, v4
	v_add_u32_e32 v4, s48, v4
	v_lshlrev_b32_e32 v4, 2, v4
	s_waitcnt lgkmcnt(0)
	global_atomic_add_f32 v4, v6, s[46:47]

.LBB3_24:
	s_or_b64 exec, exec, s[2:3]
	v_and_b32_e32 v1, 31, v0
	v_lshrrev_b32_e32 v158, 5, v156
	s_waitcnt lgkmcnt(0)
	s_barrier
	v_lshlrev_b32_e32 v250, 4, v158
	v_lshl_or_b32 v250, s13, 7, v250
	v_or_b32_e32 v254, 0x1ee00, v250
	ds_read_b128 v[168:171], v254 offset:0
	ds_read_b128 v[172:175], v254 offset:32
	ds_read_b128 v[176:179], v254 offset:64
	ds_read_b128 v[180:183], v254 offset:96
	v_bfe_u32 v255, v156, 2, 2
	v_lshl_add_u32 v250, v255, 2, v250
	v_add_u32_e32 v250, 0x1e400, v250
	s_waitcnt lgkmcnt(0)
	s_barrier
	v_mul_u32_u24_e32 v2, 0x88, v1
	s_mul_i32 s0, s16, 0x4400
	v_lshlrev_b32_e32 v2, 1, v2
	v_lshlrev_b32_e32 v3, 4, v158
	v_mov_b32_e32 v138, v0
	v_add3_u32 v159, s0, v2, v3
	ds_read_b128 v[2:5], v159
	ds_read_b128 v[18:21], v159 offset:8704
	ds_read_b128 v[130:133], v159 offset:32
	s_waitcnt vmcnt(10) lgkmcnt(2)
	v_mfma_f32_32x32x16_f16 v[50:65], v[2:5], v[126:129], 0
	s_mov_b32 s2, 0xc060c00
	s_mov_b32 s3, 0xe400
	s_mulk_i32 s16, 0x2400
	s_lshl_b32 s0, s13, 6
	s_or_b32 s0, s16, s0
	s_add_i32 s0, s0, 0x11000
	v_mul_u32_u24_e32 v251, 0x90, v1
	v_lshl_add_u32 v251, v158, 3, v251
	v_add_u32_e32 v251, s0, v251
	s_waitcnt lgkmcnt(1)
	v_mfma_f32_32x32x16_f16 v[34:49], v[18:21], v[126:129], 0
	s_or_b32 s0, s10, 2
	s_ashr_i32 s1, s0, 31
	s_lshl_b64 s[0:1], s[0:1], 12
	s_add_u32 s0, s8, s0
	s_addc_u32 s1, s9, s1
	v_cmp_gt_u32_e32 vcc, 32, v156
	v_mfma_f32_32x32x16_f16 v[2:17], v[122:125], v[2:5], v[168:183]
	v_mfma_f32_32x32x16_f16 v[18:33], v[122:125], v[18:21], v[168:183]
	ds_read_b128 v[134:137], v159 offset:8736
	ds_read_b128 v[160:163], v159 offset:64
	s_waitcnt vmcnt(8) lgkmcnt(2)
	v_mfma_f32_32x32x16_f16 v[50:65], v[130:133], v[118:121], v[50:65]
	s_waitcnt lgkmcnt(1)
	v_mfma_f32_32x32x16_f16 v[34:49], v[134:137], v[118:121], v[34:49]
	v_mfma_f32_32x32x16_f16 v[2:17], v[114:117], v[130:133], v[2:17]
	v_mfma_f32_32x32x16_f16 v[18:33], v[114:117], v[134:137], v[18:33]
	ds_read_b128 v[130:133], v159 offset:8768
	ds_read_b128 v[134:137], v159 offset:96
	s_waitcnt vmcnt(6) lgkmcnt(2)
	v_mfma_f32_32x32x16_f16 v[50:65], v[160:163], v[110:113], v[50:65]
	s_waitcnt lgkmcnt(1)
	v_mfma_f32_32x32x16_f16 v[34:49], v[130:133], v[110:113], v[34:49]
	v_mfma_f32_32x32x16_f16 v[2:17], v[106:109], v[160:163], v[2:17]
	v_mfma_f32_32x32x16_f16 v[18:33], v[106:109], v[130:133], v[18:33]
	ds_read_b128 v[130:133], v159 offset:8800
	ds_read_b128 v[160:163], v159 offset:128
	s_waitcnt vmcnt(4) lgkmcnt(2)
	v_mfma_f32_32x32x16_f16 v[50:65], v[134:137], v[102:105], v[50:65]
	s_waitcnt lgkmcnt(1)
	v_mfma_f32_32x32x16_f16 v[34:49], v[130:133], v[102:105], v[34:49]
	v_mfma_f32_32x32x16_f16 v[2:17], v[98:101], v[134:137], v[2:17]
	v_mfma_f32_32x32x16_f16 v[18:33], v[98:101], v[130:133], v[18:33]
	ds_read_b128 v[130:133], v159 offset:8832
	ds_read_b128 v[134:137], v159 offset:160
	s_waitcnt vmcnt(3) lgkmcnt(2)
	v_mfma_f32_32x32x16_f16 v[50:65], v[160:163], v[94:97], v[50:65]
	s_waitcnt lgkmcnt(1)
	v_mfma_f32_32x32x16_f16 v[34:49], v[130:133], v[94:97], v[34:49]
	v_mfma_f32_32x32x16_f16 v[2:17], v[86:89], v[160:163], v[2:17]
	v_mfma_f32_32x32x16_f16 v[18:33], v[86:89], v[130:133], v[18:33]
	ds_read_b128 v[130:133], v159 offset:8864
	ds_read_b128 v[160:163], v159 offset:192
	s_waitcnt vmcnt(2) lgkmcnt(2)
	v_mfma_f32_32x32x16_f16 v[50:65], v[134:137], v[90:93], v[50:65]
	s_waitcnt lgkmcnt(1)
	v_mfma_f32_32x32x16_f16 v[34:49], v[130:133], v[90:93], v[34:49]
	v_mfma_f32_32x32x16_f16 v[2:17], v[78:81], v[134:137], v[2:17]
	v_mfma_f32_32x32x16_f16 v[18:33], v[78:81], v[130:133], v[18:33]
	ds_read_b128 v[130:133], v159 offset:8896
	ds_read_b128 v[164:167], v159 offset:224
	s_waitcnt vmcnt(1) lgkmcnt(2)
	v_mfma_f32_32x32x16_f16 v[50:65], v[160:163], v[82:85], v[50:65]
	s_waitcnt lgkmcnt(1)
	v_mfma_f32_32x32x16_f16 v[34:49], v[130:133], v[82:85], v[34:49]
	v_mfma_f32_32x32x16_f16 v[2:17], v[70:73], v[160:163], v[2:17]
	v_mfma_f32_32x32x16_f16 v[18:33], v[70:73], v[130:133], v[18:33]
	v_lshlrev_b32_e32 v130, 3, v138
	v_and_b32_e32 v241, 0x1f8, v130
	global_load_dwordx2 v[138:139], v241, s[0:1]
	global_load_dwordx2 v[134:135], v241, s[0:1] offset:512
	global_load_dwordx2 v[132:133], v241, s[0:1] offset:1024
	global_load_dwordx2 v[130:131], v241, s[0:1] offset:1536
	global_load_dwordx2 v[136:137], v241, s[0:1] offset:2048
	s_waitcnt vmcnt(5) lgkmcnt(0)
	v_mfma_f32_32x32x16_f16 v[50:65], v[164:167], v[74:77], v[50:65]
	v_mfma_f32_32x32x16_f16 v[2:17], v[66:69], v[164:167], v[2:17]
	s_nop 10
	v_cvt_pk_f16_f32 v57, v56, v57
	v_cvt_pk_f16_f32 v56, v54, v55
	v_cvt_pk_f16_f32 v55, v52, v53
	v_cvt_pk_f16_f32 v54, v50, v51
	v_perm_b32 v50, v240, v154, s42
	v_perm_b32 v51, v240, v154, s43
	v_perm_b32 v52, v240, v155, s42
	v_perm_b32 v53, v240, v155, s43
	v_pk_add_f16 v50, v50, s3 op_sel_hi:[1,0]
	v_pk_add_f16 v51, v51, s3 op_sel_hi:[1,0]
	v_pk_add_f16 v52, v52, s3 op_sel_hi:[1,0]
	v_pk_add_f16 v53, v53, s3 op_sel_hi:[1,0]
	v_cvt_pk_f16_f32 v65, v64, v65
	v_cvt_pk_f16_f32 v64, v62, v63
	v_cvt_pk_f16_f32 v63, v60, v61
	v_cvt_pk_f16_f32 v62, v58, v59
	v_mfma_f32_32x32x16_f16 v[2:17], v[54:57], v[50:53], v[2:17]
	v_perm_b32 v58, v240, v150, s42
	v_perm_b32 v59, v240, v150, s43
	v_perm_b32 v60, v240, v151, s42
	v_perm_b32 v61, v240, v151, s43
	v_pk_add_f16 v58, v58, s3 op_sel_hi:[1,0]
	v_pk_add_f16 v59, v59, s3 op_sel_hi:[1,0]
	v_pk_add_f16 v60, v60, s3 op_sel_hi:[1,0]
	v_pk_add_f16 v61, v61, s3 op_sel_hi:[1,0]
	s_nop 1
	v_mfma_f32_32x32x16_f16 v[2:17], v[62:65], v[58:61], v[2:17]
	ds_read_b128 v[160:163], v159 offset:8928
	v_perm_b32 v155, v240, v152, s43
	v_perm_b32 v164, v240, v153, s42
	s_waitcnt lgkmcnt(0)
	v_mfma_f32_32x32x16_f16 v[18:33], v[66:69], v[160:163], v[18:33]
	v_perm_b32 v154, v240, v152, s42
	v_perm_b32 v165, v240, v153, s43
	v_pk_add_f16 v152, v154, s3 op_sel_hi:[1,0]
	v_pk_add_f16 v153, v155, s3 op_sel_hi:[1,0]
	v_pk_add_f16 v154, v164, s3 op_sel_hi:[1,0]
	v_pk_add_f16 v155, v165, s3 op_sel_hi:[1,0]
	v_mfma_f32_32x32x16_f16 v[34:49], v[160:163], v[74:77], v[34:49]
	v_perm_b32 v151, v240, v148, s43
	v_perm_b32 v164, v240, v149, s42
	v_mfma_f32_32x32x16_f16 v[18:33], v[54:57], v[152:155], v[18:33]
	v_perm_b32 v150, v240, v148, s42
	v_perm_b32 v165, v240, v149, s43
	v_pk_add_f16 v148, v150, s3 op_sel_hi:[1,0]
	v_pk_add_f16 v149, v151, s3 op_sel_hi:[1,0]
	v_pk_add_f16 v150, v164, s3 op_sel_hi:[1,0]
	v_pk_add_f16 v151, v165, s3 op_sel_hi:[1,0]
	s_nop 2
	v_cvt_pk_f16_f32 v41, v40, v41
	v_cvt_pk_f16_f32 v40, v38, v39
	v_cvt_pk_f16_f32 v38, v34, v35
	v_cvt_pk_f16_f32 v39, v36, v37
	v_mfma_f32_32x32x16_f16 v[18:33], v[62:65], v[148:151], v[18:33]
	v_perm_b32 v34, v240, v146, s42
	v_perm_b32 v35, v240, v146, s43
	v_perm_b32 v36, v240, v147, s42
	v_perm_b32 v37, v240, v147, s43
	v_pk_add_f16 v34, v34, s3 op_sel_hi:[1,0]
	v_pk_add_f16 v35, v35, s3 op_sel_hi:[1,0]
	v_pk_add_f16 v36, v36, s3 op_sel_hi:[1,0]
	v_pk_add_f16 v37, v37, s3 op_sel_hi:[1,0]
	v_perm_b32 v146, v240, v144, s42
	v_perm_b32 v144, v240, v144, s43
	v_perm_b32 v147, v240, v145, s42
	v_perm_b32 v53, v240, v145, s43
	v_pk_add_f16 v50, v146, s3 op_sel_hi:[1,0]
	v_pk_add_f16 v51, v144, s3 op_sel_hi:[1,0]
	v_pk_add_f16 v52, v147, s3 op_sel_hi:[1,0]
	v_pk_add_f16 v53, v53, s3 op_sel_hi:[1,0]
	v_cvt_pk_f16_f32 v49, v48, v49
	v_cvt_pk_f16_f32 v48, v46, v47
	v_cvt_pk_f16_f32 v47, v44, v45
	v_mfma_f32_32x32x16_f16 v[2:17], v[38:41], v[34:37], v[2:17]
	v_cvt_pk_f16_f32 v46, v42, v43
	v_mfma_f32_32x32x16_f16 v[18:33], v[38:41], v[50:53], v[18:33]
	v_perm_b32 v34, v240, v140, s42
	v_perm_b32 v35, v240, v140, s43
	v_perm_b32 v36, v240, v141, s42
	v_perm_b32 v37, v240, v141, s43
	v_perm_b32 v42, v240, v142, s42
	v_perm_b32 v43, v240, v142, s43
	v_perm_b32 v44, v240, v143, s42
	v_perm_b32 v45, v240, v143, s43
	v_pk_add_f16 v34, v34, s3 op_sel_hi:[1,0]
	v_pk_add_f16 v35, v35, s3 op_sel_hi:[1,0]
	v_pk_add_f16 v36, v36, s3 op_sel_hi:[1,0]
	v_pk_add_f16 v37, v37, s3 op_sel_hi:[1,0]
	v_pk_add_f16 v42, v42, s3 op_sel_hi:[1,0]
	v_pk_add_f16 v43, v43, s3 op_sel_hi:[1,0]
	v_pk_add_f16 v44, v44, s3 op_sel_hi:[1,0]
	v_pk_add_f16 v45, v45, s3 op_sel_hi:[1,0]
	v_mfma_f32_32x32x16_f16 v[18:33], v[46:49], v[34:37], v[18:33]
	global_load_dwordx2 v[154:155], v241, s[0:1] offset:2560
	global_load_dwordx2 v[152:153], v241, s[0:1] offset:3072
	global_load_dwordx2 v[150:151], v241, s[0:1] offset:3584
	v_mov_b32_e32 v148, v0
	s_or_b32 s0, s10, 4
	s_ashr_i32 s1, s0, 31
	s_lshl_b64 s[0:1], s[0:1], 12
	v_mfma_f32_32x32x16_f16 v[2:17], v[46:49], v[42:45], v[2:17]
	s_nop 7
	s_nop 4
	v_cvt_pk_f16_f32 v254, v2, v3
	v_cvt_pk_f16_f32 v255, v4, v5
	ds_write_b64 v251, v[254:255] offset:0
	v_cvt_pk_f16_f32 v252, v6, v7
	v_cvt_pk_f16_f32 v253, v8, v9
	ds_write_b64 v251, v[252:253] offset:16
	v_cvt_pk_f16_f32 v254, v10, v11
	v_cvt_pk_f16_f32 v255, v12, v13
	ds_write_b64 v251, v[254:255] offset:32
	v_cvt_pk_f16_f32 v252, v14, v15
	v_cvt_pk_f16_f32 v253, v16, v17
	ds_write_b64 v251, v[252:253] offset:48
	v_cvt_pk_f16_f32 v254, v18, v19
	v_cvt_pk_f16_f32 v255, v20, v21
	ds_write_b64 v251, v[254:255] offset:4608
	v_pk_add_f32 v[222:223], v[2:3], v[18:19]
	v_pk_mul_f32 v[194:195], v[2:3], v[2:3]
	v_pk_fma_f32 v[194:195], v[18:19], v[18:19], v[194:195]
	v_pk_add_f32 v[220:221], v[4:5], v[20:21]
	v_pk_mul_f32 v[192:193], v[4:5], v[4:5]
	v_pk_fma_f32 v[192:193], v[20:21], v[20:21], v[192:193]
	v_cvt_pk_f16_f32 v252, v22, v23
	v_cvt_pk_f16_f32 v253, v24, v25
	ds_write_b64 v251, v[252:253] offset:4624
	v_pk_add_f32 v[218:219], v[6:7], v[22:23]
	v_pk_mul_f32 v[184:185], v[6:7], v[6:7]
	v_pk_fma_f32 v[184:185], v[22:23], v[22:23], v[184:185]
	v_pk_add_f32 v[216:217], v[8:9], v[24:25]
	v_pk_mul_f32 v[166:167], v[8:9], v[8:9]
	v_pk_fma_f32 v[166:167], v[24:25], v[24:25], v[166:167]
	v_cvt_pk_f16_f32 v254, v26, v27
	v_cvt_pk_f16_f32 v255, v28, v29
	ds_write_b64 v251, v[254:255] offset:4640
	v_pk_add_f32 v[214:215], v[10:11], v[26:27]
	v_pk_mul_f32 v[164:165], v[10:11], v[10:11]
	v_pk_fma_f32 v[164:165], v[26:27], v[26:27], v[164:165]
	v_pk_add_f32 v[204:205], v[12:13], v[28:29]
	v_pk_mul_f32 v[162:163], v[12:13], v[12:13]
	v_pk_fma_f32 v[162:163], v[28:29], v[28:29], v[162:163]
	v_cvt_pk_f16_f32 v252, v30, v31
	v_cvt_pk_f16_f32 v253, v32, v33
	ds_write_b64 v251, v[252:253] offset:4656
	v_pk_add_f32 v[202:203], v[14:15], v[30:31]
	v_pk_mul_f32 v[160:161], v[14:15], v[14:15]
	v_pk_fma_f32 v[160:161], v[30:31], v[30:31], v[160:161]
	v_pk_add_f32 v[196:197], v[16:17], v[32:33]
	v_pk_mul_f32 v[156:157], v[16:17], v[16:17]
	v_pk_fma_f32 v[156:157], v[32:33], v[32:33], v[156:157]
	s_nop 3
	s_nop 0
	s_waitcnt lgkmcnt(0)
	s_barrier
	s_nop 4
	ds_read_b128 v[2:5], v159 offset:34816
	ds_read_b128 v[18:21], v159 offset:43520
	ds_read_b128 v[140:143], v159 offset:34848
	ds_read_b128 v[144:147], v159 offset:43552
	s_waitcnt lgkmcnt(3)
	v_mfma_f32_32x32x16_f16 v[50:65], v[2:5], v[126:129], 0
	s_add_u32 s0, s8, s0
	s_addc_u32 s1, s9, s1
	s_waitcnt lgkmcnt(2)
	v_mfma_f32_32x32x16_f16 v[34:49], v[18:21], v[126:129], 0
	v_mfma_f32_32x32x16_f16 v[2:17], v[122:125], v[2:5], v[168:183]
	v_mfma_f32_32x32x16_f16 v[18:33], v[122:125], v[18:21], v[168:183]
	ds_read_b128 v[242:245], v159 offset:34880
	ds_read_b128 v[246:249], v159 offset:43584
	s_waitcnt lgkmcnt(3)
	v_mfma_f32_32x32x16_f16 v[50:65], v[140:143], v[118:121], v[50:65]
	s_waitcnt lgkmcnt(2)
	v_mfma_f32_32x32x16_f16 v[34:49], v[144:147], v[118:121], v[34:49]
	v_mfma_f32_32x32x16_f16 v[2:17], v[114:117], v[140:143], v[2:17]
	v_mfma_f32_32x32x16_f16 v[18:33], v[114:117], v[144:147], v[18:33]
	ds_read_b128 v[140:143], v159 offset:34912
	ds_read_b128 v[144:147], v159 offset:43616
	s_waitcnt lgkmcnt(3)
	v_mfma_f32_32x32x16_f16 v[50:65], v[242:245], v[110:113], v[50:65]
	s_waitcnt lgkmcnt(2)
	v_mfma_f32_32x32x16_f16 v[34:49], v[246:249], v[110:113], v[34:49]
	v_mfma_f32_32x32x16_f16 v[2:17], v[106:109], v[242:245], v[2:17]
	v_mfma_f32_32x32x16_f16 v[18:33], v[106:109], v[246:249], v[18:33]
	ds_read_b128 v[242:245], v159 offset:34944
	ds_read_b128 v[246:249], v159 offset:43648
	s_waitcnt lgkmcnt(3)
	v_mfma_f32_32x32x16_f16 v[50:65], v[140:143], v[102:105], v[50:65]
	s_waitcnt lgkmcnt(2)
	v_mfma_f32_32x32x16_f16 v[34:49], v[144:147], v[102:105], v[34:49]
	v_mfma_f32_32x32x16_f16 v[2:17], v[98:101], v[140:143], v[2:17]
	v_mfma_f32_32x32x16_f16 v[18:33], v[98:101], v[144:147], v[18:33]
	ds_read_b128 v[186:189], v159 offset:34976
	ds_read_b128 v[206:209], v159 offset:43680
	s_waitcnt lgkmcnt(3)
	v_mfma_f32_32x32x16_f16 v[50:65], v[242:245], v[94:97], v[50:65]
	s_waitcnt lgkmcnt(2)
	v_mfma_f32_32x32x16_f16 v[34:49], v[246:249], v[94:97], v[34:49]
	v_mfma_f32_32x32x16_f16 v[2:17], v[86:89], v[242:245], v[2:17]
	v_mfma_f32_32x32x16_f16 v[18:33], v[86:89], v[246:249], v[18:33]
	ds_read_b128 v[140:143], v159 offset:35008
	ds_read_b128 v[144:147], v159 offset:43712
	s_waitcnt lgkmcnt(3)
	v_mfma_f32_32x32x16_f16 v[50:65], v[186:189], v[90:93], v[50:65]
	s_waitcnt lgkmcnt(2)
	v_mfma_f32_32x32x16_f16 v[34:49], v[206:209], v[90:93], v[34:49]
	v_mfma_f32_32x32x16_f16 v[2:17], v[78:81], v[186:189], v[2:17]
	v_mfma_f32_32x32x16_f16 v[18:33], v[78:81], v[206:209], v[18:33]
	ds_read_b128 v[186:189], v159 offset:35040
	ds_read_b128 v[206:209], v159 offset:43744
	s_waitcnt lgkmcnt(3)
	v_mfma_f32_32x32x16_f16 v[50:65], v[140:143], v[82:85], v[50:65]
	s_waitcnt lgkmcnt(2)
	v_mfma_f32_32x32x16_f16 v[34:49], v[144:147], v[82:85], v[34:49]
	v_mfma_f32_32x32x16_f16 v[2:17], v[70:73], v[140:143], v[2:17]
	v_lshlrev_b32_e32 v140, 3, v148
	v_and_b32_e32 v199, 0x1f8, v140
	global_load_dwordx2 v[148:149], v199, s[0:1]
	global_load_dwordx2 v[142:143], v199, s[0:1] offset:1024
	global_load_dwordx2 v[140:141], v199, s[0:1] offset:1536
	v_mfma_f32_32x32x16_f16 v[18:33], v[70:73], v[144:147], v[18:33]
	global_load_dwordx2 v[144:145], v199, s[0:1] offset:512
	global_load_dwordx2 v[146:147], v199, s[0:1] offset:2048
	s_waitcnt lgkmcnt(1)
	v_mfma_f32_32x32x16_f16 v[50:65], v[186:189], v[74:77], v[50:65]
	v_mfma_f32_32x32x16_f16 v[2:17], v[66:69], v[186:189], v[2:17]
	s_nop 10
	v_cvt_pk_f16_f32 v57, v56, v57
	v_cvt_pk_f16_f32 v56, v54, v55
	v_cvt_pk_f16_f32 v54, v50, v51
	s_waitcnt vmcnt(12)
	v_cvt_pk_f16_f32 v55, v52, v53
	s_waitcnt vmcnt(8)
	v_perm_b32 v50, v240, v138, s42
	v_perm_b32 v51, v240, v138, s43
	v_perm_b32 v52, v240, v139, s42
	v_perm_b32 v53, v240, v139, s43
	v_perm_b32 v139, v240, v136, s43
	v_pk_add_f16 v50, v50, s3 op_sel_hi:[1,0]
	v_pk_add_f16 v51, v51, s3 op_sel_hi:[1,0]
	v_pk_add_f16 v52, v52, s3 op_sel_hi:[1,0]
	v_pk_add_f16 v53, v53, s3 op_sel_hi:[1,0]
	v_perm_b32 v190, v240, v137, s42
	s_waitcnt lgkmcnt(0)
	v_mfma_f32_32x32x16_f16 v[18:33], v[66:69], v[206:209], v[18:33]
	v_perm_b32 v138, v240, v136, s42
	v_perm_b32 v191, v240, v137, s43
	v_pk_add_f16 v136, v138, s3 op_sel_hi:[1,0]
	v_pk_add_f16 v137, v139, s3 op_sel_hi:[1,0]
	v_pk_add_f16 v138, v190, s3 op_sel_hi:[1,0]
	v_pk_add_f16 v139, v191, s3 op_sel_hi:[1,0]
	v_cvt_pk_f16_f32 v65, v64, v65
	v_cvt_pk_f16_f32 v64, v62, v63
	v_cvt_pk_f16_f32 v63, v60, v61
	v_cvt_pk_f16_f32 v62, v58, v59
	v_mfma_f32_32x32x16_f16 v[34:49], v[206:209], v[74:77], v[34:49]
	v_mfma_f32_32x32x16_f16 v[2:17], v[54:57], v[50:53], v[2:17]
	s_waitcnt vmcnt(7)
	v_perm_b32 v58, v240, v134, s42
	v_perm_b32 v59, v240, v134, s43
	v_perm_b32 v60, v240, v135, s42
	v_perm_b32 v61, v240, v135, s43
	v_pk_add_f16 v58, v58, s3 op_sel_hi:[1,0]
	v_pk_add_f16 v59, v59, s3 op_sel_hi:[1,0]
	v_pk_add_f16 v60, v60, s3 op_sel_hi:[1,0]
	v_pk_add_f16 v61, v61, s3 op_sel_hi:[1,0]
	v_mfma_f32_32x32x16_f16 v[18:33], v[54:57], v[136:139], v[18:33]
	v_perm_b32 v134, v240, v154, s42
	v_perm_b32 v135, v240, v154, s43
	v_perm_b32 v154, v240, v155, s42
	v_perm_b32 v155, v240, v155, s43
	v_pk_add_f16 v210, v134, s3 op_sel_hi:[1,0]
	v_pk_add_f16 v211, v135, s3 op_sel_hi:[1,0]
	v_pk_add_f16 v212, v154, s3 op_sel_hi:[1,0]
	v_pk_add_f16 v213, v155, s3 op_sel_hi:[1,0]
	v_cvt_pk_f16_f32 v41, v40, v41
	v_cvt_pk_f16_f32 v40, v38, v39
	v_cvt_pk_f16_f32 v39, v36, v37
	v_cvt_pk_f16_f32 v38, v34, v35
	v_mfma_f32_32x32x16_f16 v[2:17], v[62:65], v[58:61], v[2:17]
	v_perm_b32 v34, v240, v132, s42
	v_perm_b32 v35, v240, v132, s43
	v_perm_b32 v36, v240, v133, s42
	v_perm_b32 v37, v240, v133, s43
	v_pk_add_f16 v34, v34, s3 op_sel_hi:[1,0]
	v_pk_add_f16 v35, v35, s3 op_sel_hi:[1,0]
	v_pk_add_f16 v36, v36, s3 op_sel_hi:[1,0]
	v_pk_add_f16 v37, v37, s3 op_sel_hi:[1,0]
	s_waitcnt vmcnt(6)
	v_mfma_f32_32x32x16_f16 v[18:33], v[62:65], v[210:213], v[18:33]
	v_perm_b32 v132, v240, v152, s42
	v_perm_b32 v133, v240, v152, s43
	v_perm_b32 v134, v240, v153, s42
	v_perm_b32 v53, v240, v153, s43
	v_pk_add_f16 v50, v132, s3 op_sel_hi:[1,0]
	v_pk_add_f16 v51, v133, s3 op_sel_hi:[1,0]
	v_pk_add_f16 v52, v134, s3 op_sel_hi:[1,0]
	v_pk_add_f16 v53, v53, s3 op_sel_hi:[1,0]
	v_cvt_pk_f16_f32 v49, v48, v49
	v_cvt_pk_f16_f32 v48, v46, v47
	v_cvt_pk_f16_f32 v47, v44, v45
	v_cvt_pk_f16_f32 v46, v42, v43
	v_mfma_f32_32x32x16_f16 v[2:17], v[38:41], v[34:37], v[2:17]
	v_perm_b32 v42, v240, v130, s42
	v_perm_b32 v43, v240, v130, s43
	v_perm_b32 v44, v240, v131, s42
	v_perm_b32 v45, v240, v131, s43
	v_pk_add_f16 v42, v42, s3 op_sel_hi:[1,0]
	v_pk_add_f16 v43, v43, s3 op_sel_hi:[1,0]
	v_pk_add_f16 v44, v44, s3 op_sel_hi:[1,0]
	v_pk_add_f16 v45, v45, s3 op_sel_hi:[1,0]
	s_waitcnt vmcnt(5)
	v_mfma_f32_32x32x16_f16 v[18:33], v[38:41], v[50:53], v[18:33]
	v_perm_b32 v34, v240, v150, s42
	v_perm_b32 v35, v240, v150, s43
	v_perm_b32 v36, v240, v151, s42
	v_perm_b32 v37, v240, v151, s43
	v_pk_add_f16 v34, v34, s3 op_sel_hi:[1,0]
	v_pk_add_f16 v35, v35, s3 op_sel_hi:[1,0]
	v_pk_add_f16 v36, v36, s3 op_sel_hi:[1,0]
	v_pk_add_f16 v37, v37, s3 op_sel_hi:[1,0]
	v_mfma_f32_32x32x16_f16 v[2:17], v[46:49], v[42:45], v[2:17]
	global_load_dwordx2 v[154:155], v199, s[0:1] offset:2560
	global_load_dwordx2 v[152:153], v199, s[0:1] offset:3072
	global_load_dwordx2 v[150:151], v199, s[0:1] offset:3584
	s_or_b32 s0, s10, 6
	s_ashr_i32 s1, s0, 31
	s_lshl_b64 s[0:1], s[0:1], 12
	s_add_u32 s0, s8, s0
	v_mfma_f32_32x32x16_f16 v[18:33], v[46:49], v[34:37], v[18:33]
	s_nop 7
	s_nop 4
	v_cvt_pk_f16_f32 v254, v2, v3
	v_cvt_pk_f16_f32 v255, v4, v5
	ds_write_b64 v251, v[254:255] offset:18432
	v_pk_add_f32 v[222:223], v[222:223], v[2:3]
	v_pk_fma_f32 v[194:195], v[2:3], v[2:3], v[194:195]
	v_pk_add_f32 v[220:221], v[220:221], v[4:5]
	v_pk_fma_f32 v[192:193], v[4:5], v[4:5], v[192:193]
	v_cvt_pk_f16_f32 v252, v6, v7
	v_cvt_pk_f16_f32 v253, v8, v9
	ds_write_b64 v251, v[252:253] offset:18448
	v_pk_add_f32 v[218:219], v[218:219], v[6:7]
	v_pk_fma_f32 v[184:185], v[6:7], v[6:7], v[184:185]
	v_pk_add_f32 v[216:217], v[216:217], v[8:9]
	v_pk_fma_f32 v[166:167], v[8:9], v[8:9], v[166:167]
	v_cvt_pk_f16_f32 v254, v10, v11
	v_cvt_pk_f16_f32 v255, v12, v13
	ds_write_b64 v251, v[254:255] offset:18464
	v_pk_add_f32 v[214:215], v[214:215], v[10:11]
	v_pk_fma_f32 v[164:165], v[10:11], v[10:11], v[164:165]
	v_pk_add_f32 v[204:205], v[204:205], v[12:13]
	v_pk_fma_f32 v[162:163], v[12:13], v[12:13], v[162:163]
	v_cvt_pk_f16_f32 v252, v14, v15
	v_cvt_pk_f16_f32 v253, v16, v17
	ds_write_b64 v251, v[252:253] offset:18480
	v_pk_add_f32 v[202:203], v[202:203], v[14:15]
	v_pk_fma_f32 v[160:161], v[14:15], v[14:15], v[160:161]
	v_pk_add_f32 v[196:197], v[196:197], v[16:17]
	v_pk_fma_f32 v[156:157], v[16:17], v[16:17], v[156:157]
	v_cvt_pk_f16_f32 v254, v18, v19
	v_cvt_pk_f16_f32 v255, v20, v21
	ds_write_b64 v251, v[254:255] offset:23040
	v_pk_add_f32 v[222:223], v[222:223], v[18:19]
	v_pk_fma_f32 v[194:195], v[18:19], v[18:19], v[194:195]
	v_pk_add_f32 v[220:221], v[220:221], v[20:21]
	v_pk_fma_f32 v[192:193], v[20:21], v[20:21], v[192:193]
	v_cvt_pk_f16_f32 v252, v22, v23
	v_cvt_pk_f16_f32 v253, v24, v25
	ds_write_b64 v251, v[252:253] offset:23056
	v_pk_add_f32 v[218:219], v[218:219], v[22:23]
	v_pk_fma_f32 v[184:185], v[22:23], v[22:23], v[184:185]
	v_pk_add_f32 v[216:217], v[216:217], v[24:25]
	v_pk_fma_f32 v[166:167], v[24:25], v[24:25], v[166:167]
	v_cvt_pk_f16_f32 v254, v26, v27
	v_cvt_pk_f16_f32 v255, v28, v29
	ds_write_b64 v251, v[254:255] offset:23072
	v_pk_add_f32 v[214:215], v[214:215], v[26:27]
	v_pk_fma_f32 v[164:165], v[26:27], v[26:27], v[164:165]
	v_pk_add_f32 v[204:205], v[204:205], v[28:29]
	v_pk_fma_f32 v[162:163], v[28:29], v[28:29], v[162:163]
	v_cvt_pk_f16_f32 v252, v30, v31
	v_cvt_pk_f16_f32 v253, v32, v33
	ds_write_b64 v251, v[252:253] offset:23088
	v_pk_add_f32 v[202:203], v[202:203], v[30:31]
	v_pk_fma_f32 v[160:161], v[30:31], v[30:31], v[160:161]
	v_pk_add_f32 v[196:197], v[196:197], v[32:33]
	v_pk_fma_f32 v[156:157], v[32:33], v[32:33], v[156:157]
	s_nop 3
	s_nop 0
	s_nop 0
	s_waitcnt lgkmcnt(0)
	s_barrier
	ds_read_b128 v[2:5], v159
	s_nop 2
	ds_read_b128 v[18:21], v159 offset:8704
	s_waitcnt lgkmcnt(1)
	v_mfma_f32_32x32x16_f16 v[50:65], v[2:5], v[126:129], 0
	v_lshlrev_b32_e32 v0, 3, v0
	s_addc_u32 s1, s9, s1
	v_and_b32_e32 v0, 0x1f8, v0
	global_load_dwordx2 v[138:139], v0, s[0:1]
	s_waitcnt lgkmcnt(0)
	v_mfma_f32_32x32x16_f16 v[34:49], v[18:21], v[126:129], 0
	v_mfma_f32_32x32x16_f16 v[2:17], v[122:125], v[2:5], v[168:183]
	v_mfma_f32_32x32x16_f16 v[18:33], v[122:125], v[18:21], v[168:183]
	ds_read_b128 v[130:133], v159 offset:32
	ds_read_b128 v[134:137], v159 offset:8736
	s_waitcnt lgkmcnt(1)
	v_mfma_f32_32x32x16_f16 v[50:65], v[130:133], v[118:121], v[50:65]
	s_waitcnt lgkmcnt(0)
	v_mfma_f32_32x32x16_f16 v[34:49], v[134:137], v[118:121], v[34:49]
	v_mfma_f32_32x32x16_f16 v[2:17], v[114:117], v[130:133], v[2:17]
	v_mfma_f32_32x32x16_f16 v[18:33], v[114:117], v[134:137], v[18:33]
	ds_read_b128 v[224:227], v159 offset:64
	ds_read_b128 v[228:231], v159 offset:8768
	ds_read_b128 v[130:133], v159 offset:96
	ds_read_b128 v[134:137], v159 offset:8800
	s_waitcnt lgkmcnt(3)
	v_mfma_f32_32x32x16_f16 v[50:65], v[224:227], v[110:113], v[50:65]
	s_waitcnt lgkmcnt(2)
	v_mfma_f32_32x32x16_f16 v[34:49], v[228:231], v[110:113], v[34:49]
	v_mfma_f32_32x32x16_f16 v[2:17], v[106:109], v[224:227], v[2:17]
	v_mfma_f32_32x32x16_f16 v[18:33], v[106:109], v[228:231], v[18:33]
	ds_read_b128 v[224:227], v159 offset:128
	ds_read_b128 v[228:231], v159 offset:8832
	s_waitcnt lgkmcnt(3)
	v_mfma_f32_32x32x16_f16 v[50:65], v[130:133], v[102:105], v[50:65]
	s_waitcnt lgkmcnt(2)
	v_mfma_f32_32x32x16_f16 v[34:49], v[134:137], v[102:105], v[34:49]
	v_mfma_f32_32x32x16_f16 v[2:17], v[98:101], v[130:133], v[2:17]
	v_mfma_f32_32x32x16_f16 v[18:33], v[98:101], v[134:137], v[18:33]
	ds_read_b128 v[130:133], v159 offset:160
	ds_read_b128 v[134:137], v159 offset:8864
	s_waitcnt lgkmcnt(3)
	v_mfma_f32_32x32x16_f16 v[50:65], v[224:227], v[94:97], v[50:65]
	s_waitcnt lgkmcnt(2)
	v_mfma_f32_32x32x16_f16 v[34:49], v[228:231], v[94:97], v[34:49]
	v_mfma_f32_32x32x16_f16 v[2:17], v[86:89], v[224:227], v[2:17]
	v_mfma_f32_32x32x16_f16 v[18:33], v[86:89], v[228:231], v[18:33]
	ds_read_b128 v[224:227], v159 offset:192
	ds_read_b128 v[228:231], v159 offset:8896
	s_waitcnt lgkmcnt(3)
	v_mfma_f32_32x32x16_f16 v[50:65], v[130:133], v[90:93], v[50:65]
	s_waitcnt lgkmcnt(2)
	v_mfma_f32_32x32x16_f16 v[34:49], v[134:137], v[90:93], v[34:49]
	v_mfma_f32_32x32x16_f16 v[2:17], v[78:81], v[130:133], v[2:17]
	v_mfma_f32_32x32x16_f16 v[18:33], v[78:81], v[134:137], v[18:33]
	ds_read_b128 v[232:235], v159 offset:224
	ds_read_b128 v[236:239], v159 offset:8928
	s_waitcnt lgkmcnt(3)
	v_mfma_f32_32x32x16_f16 v[50:65], v[224:227], v[82:85], v[50:65]
	global_load_dwordx2 v[134:135], v0, s[0:1] offset:512
	global_load_dwordx2 v[132:133], v0, s[0:1] offset:1024
	global_load_dwordx2 v[130:131], v0, s[0:1] offset:1536
	s_waitcnt lgkmcnt(2)
	v_mfma_f32_32x32x16_f16 v[34:49], v[228:231], v[82:85], v[34:49]
	global_load_dwordx2 v[136:137], v0, s[0:1] offset:2048
	v_mfma_f32_32x32x16_f16 v[2:17], v[70:73], v[224:227], v[2:17]
	v_mfma_f32_32x32x16_f16 v[18:33], v[70:73], v[228:231], v[18:33]
	s_waitcnt lgkmcnt(1)
	v_mfma_f32_32x32x16_f16 v[50:65], v[232:235], v[74:77], v[50:65]
	v_mfma_f32_32x32x16_f16 v[2:17], v[66:69], v[232:235], v[2:17]
	s_nop 10
	v_cvt_pk_f16_f32 v57, v56, v57
	v_cvt_pk_f16_f32 v56, v54, v55
	v_cvt_pk_f16_f32 v54, v50, v51
	s_waitcnt vmcnt(12)
	v_lshlrev_b32_e32 v50, 8, v148
	v_cvt_pk_f16_f32 v55, v52, v53
	v_perm_b32 v50, v50, v148, s2
	v_lshrrev_b32_e32 v51, 16, v148
	v_lshrrev_b32_e32 v52, 8, v148
	v_lshrrev_b32_e32 v53, 16, v149
	v_lshrrev_b32_e32 v148, 8, v149
	v_perm_b32 v51, v52, v51, s2
	v_lshlrev_b32_e32 v52, 8, v149
	v_perm_b32 v53, v148, v53, s2
	s_waitcnt vmcnt(8)
	v_perm_b32 v52, v52, v149, s2
	v_perm_b32 v149, v240, v146, s43
	v_perm_b32 v198, v240, v147, s42
	s_waitcnt lgkmcnt(0)
	v_mfma_f32_32x32x16_f16 v[18:33], v[66:69], v[236:239], v[18:33]
	v_or_b32_e32 v50, 0x64006400, v50
	v_or_b32_e32 v51, 0x64006400, v51
	v_or_b32_e32 v52, 0x64006400, v52
	v_or_b32_e32 v53, 0x64006400, v53
	v_pk_add_f16 v50, v50, s3 op_sel_hi:[1,0]
	v_pk_add_f16 v51, v51, s3 op_sel_hi:[1,0]
	v_pk_add_f16 v52, v52, s3 op_sel_hi:[1,0]
	v_pk_add_f16 v53, v53, s3 op_sel_hi:[1,0]
	v_perm_b32 v148, v240, v146, s42
	v_perm_b32 v200, v240, v147, s43
	v_pk_add_f16 v146, v148, s3 op_sel_hi:[1,0]
	v_pk_add_f16 v147, v149, s3 op_sel_hi:[1,0]
	v_pk_add_f16 v148, v198, s3 op_sel_hi:[1,0]
	v_pk_add_f16 v149, v200, s3 op_sel_hi:[1,0]
	v_cvt_pk_f16_f32 v65, v64, v65
	v_cvt_pk_f16_f32 v64, v62, v63
	v_cvt_pk_f16_f32 v62, v58, v59
	v_cvt_pk_f16_f32 v63, v60, v61
	s_waitcnt vmcnt(7)
	v_mfma_f32_32x32x16_f16 v[34:49], v[236:239], v[74:77], v[34:49]
	v_mfma_f32_32x32x16_f16 v[2:17], v[54:57], v[50:53], v[2:17]
	v_perm_b32 v58, v240, v144, s42
	v_perm_b32 v59, v240, v144, s43
	v_perm_b32 v60, v240, v145, s42
	v_perm_b32 v61, v240, v145, s43
	v_mfma_f32_32x32x16_f16 v[18:33], v[54:57], v[146:149], v[18:33]
	v_pk_add_f16 v58, v58, s3 op_sel_hi:[1,0]
	v_pk_add_f16 v59, v59, s3 op_sel_hi:[1,0]
	v_pk_add_f16 v60, v60, s3 op_sel_hi:[1,0]
	v_pk_add_f16 v61, v61, s3 op_sel_hi:[1,0]
	v_perm_b32 v144, v240, v154, s42
	v_perm_b32 v145, v240, v154, s43
	v_perm_b32 v154, v240, v155, s42
	v_perm_b32 v155, v240, v155, s43
	v_pk_add_f16 v224, v144, s3 op_sel_hi:[1,0]
	v_pk_add_f16 v225, v145, s3 op_sel_hi:[1,0]
	v_pk_add_f16 v226, v154, s3 op_sel_hi:[1,0]
	v_pk_add_f16 v227, v155, s3 op_sel_hi:[1,0]
	v_cvt_pk_f16_f32 v41, v40, v41
	v_cvt_pk_f16_f32 v40, v38, v39
	v_cvt_pk_f16_f32 v39, v36, v37
	v_cvt_pk_f16_f32 v38, v34, v35
	s_waitcnt vmcnt(6)
	v_mfma_f32_32x32x16_f16 v[2:17], v[62:65], v[58:61], v[2:17]
	v_perm_b32 v34, v240, v142, s42
	v_perm_b32 v35, v240, v142, s43
	v_mfma_f32_32x32x16_f16 v[18:33], v[62:65], v[224:227], v[18:33]
	v_perm_b32 v36, v240, v143, s42
	v_perm_b32 v37, v240, v143, s43
	v_pk_add_f16 v34, v34, s3 op_sel_hi:[1,0]
	v_pk_add_f16 v35, v35, s3 op_sel_hi:[1,0]
	v_pk_add_f16 v36, v36, s3 op_sel_hi:[1,0]
	v_pk_add_f16 v37, v37, s3 op_sel_hi:[1,0]
	v_perm_b32 v142, v240, v152, s42
	v_perm_b32 v143, v240, v152, s43
	v_perm_b32 v144, v240, v153, s42
	v_perm_b32 v53, v240, v153, s43
	v_pk_add_f16 v50, v142, s3 op_sel_hi:[1,0]
	v_pk_add_f16 v51, v143, s3 op_sel_hi:[1,0]
	v_pk_add_f16 v52, v144, s3 op_sel_hi:[1,0]
	v_pk_add_f16 v53, v53, s3 op_sel_hi:[1,0]
	v_cvt_pk_f16_f32 v49, v48, v49
	v_cvt_pk_f16_f32 v48, v46, v47
	v_cvt_pk_f16_f32 v47, v44, v45
	v_cvt_pk_f16_f32 v46, v42, v43
	v_mfma_f32_32x32x16_f16 v[2:17], v[38:41], v[34:37], v[2:17]
	s_waitcnt vmcnt(5)
	v_mfma_f32_32x32x16_f16 v[18:33], v[38:41], v[50:53], v[18:33]
	v_perm_b32 v42, v240, v140, s42
	v_perm_b32 v43, v240, v140, s43
	v_perm_b32 v44, v240, v141, s42
	v_perm_b32 v45, v240, v141, s43
	v_perm_b32 v34, v240, v150, s42
	v_perm_b32 v35, v240, v150, s43
	v_perm_b32 v36, v240, v151, s42
	v_perm_b32 v37, v240, v151, s43
	v_pk_add_f16 v42, v42, s3 op_sel_hi:[1,0]
	v_pk_add_f16 v43, v43, s3 op_sel_hi:[1,0]
	v_pk_add_f16 v44, v44, s3 op_sel_hi:[1,0]
	v_pk_add_f16 v45, v45, s3 op_sel_hi:[1,0]
	v_pk_add_f16 v34, v34, s3 op_sel_hi:[1,0]
	v_pk_add_f16 v35, v35, s3 op_sel_hi:[1,0]
	v_pk_add_f16 v36, v36, s3 op_sel_hi:[1,0]
	v_pk_add_f16 v37, v37, s3 op_sel_hi:[1,0]
	v_mfma_f32_32x32x16_f16 v[2:17], v[46:49], v[42:45], v[2:17]
	global_load_dwordx2 v[142:143], v0, s[0:1] offset:2560
	global_load_dwordx2 v[140:141], v0, s[0:1] offset:3072
	global_load_dwordx2 v[64:65], v0, s[0:1] offset:3584
	v_mfma_f32_32x32x16_f16 v[18:33], v[46:49], v[34:37], v[18:33]
	s_nop 7
	s_nop 4
	v_cvt_pk_f16_f32 v254, v2, v3
	v_cvt_pk_f16_f32 v255, v4, v5
	ds_write_b64 v251, v[254:255] offset:0
	v_pk_add_f32 v[222:223], v[222:223], v[2:3]
	v_pk_fma_f32 v[194:195], v[2:3], v[2:3], v[194:195]
	v_pk_add_f32 v[220:221], v[220:221], v[4:5]
	v_pk_fma_f32 v[192:193], v[4:5], v[4:5], v[192:193]
	v_cvt_pk_f16_f32 v252, v6, v7
	v_cvt_pk_f16_f32 v253, v8, v9
	ds_write_b64 v251, v[252:253] offset:16
	v_pk_add_f32 v[218:219], v[218:219], v[6:7]
	v_pk_fma_f32 v[184:185], v[6:7], v[6:7], v[184:185]
	v_pk_add_f32 v[216:217], v[216:217], v[8:9]
	v_pk_fma_f32 v[166:167], v[8:9], v[8:9], v[166:167]
	v_cvt_pk_f16_f32 v254, v10, v11
	v_cvt_pk_f16_f32 v255, v12, v13
	ds_write_b64 v251, v[254:255] offset:32
	v_pk_add_f32 v[214:215], v[214:215], v[10:11]
	v_pk_fma_f32 v[164:165], v[10:11], v[10:11], v[164:165]
	v_pk_add_f32 v[204:205], v[204:205], v[12:13]
	v_pk_fma_f32 v[162:163], v[12:13], v[12:13], v[162:163]
	v_cvt_pk_f16_f32 v252, v14, v15
	v_cvt_pk_f16_f32 v253, v16, v17
	ds_write_b64 v251, v[252:253] offset:48
	v_pk_add_f32 v[202:203], v[202:203], v[14:15]
	v_pk_fma_f32 v[160:161], v[14:15], v[14:15], v[160:161]
	v_pk_add_f32 v[196:197], v[196:197], v[16:17]
	v_pk_fma_f32 v[156:157], v[16:17], v[16:17], v[156:157]
	v_cvt_pk_f16_f32 v254, v18, v19
	v_cvt_pk_f16_f32 v255, v20, v21
	ds_write_b64 v251, v[254:255] offset:4608
	v_pk_add_f32 v[222:223], v[222:223], v[18:19]
	v_pk_fma_f32 v[194:195], v[18:19], v[18:19], v[194:195]
	v_pk_add_f32 v[220:221], v[220:221], v[20:21]
	v_pk_fma_f32 v[192:193], v[20:21], v[20:21], v[192:193]
	v_cvt_pk_f16_f32 v252, v22, v23
	v_cvt_pk_f16_f32 v253, v24, v25
	ds_write_b64 v251, v[252:253] offset:4624
	v_pk_add_f32 v[218:219], v[218:219], v[22:23]
	v_pk_fma_f32 v[184:185], v[22:23], v[22:23], v[184:185]
	v_pk_add_f32 v[216:217], v[216:217], v[24:25]
	v_pk_fma_f32 v[166:167], v[24:25], v[24:25], v[166:167]
	v_cvt_pk_f16_f32 v254, v26, v27
	v_cvt_pk_f16_f32 v255, v28, v29
	ds_write_b64 v251, v[254:255] offset:4640
	v_pk_add_f32 v[214:215], v[214:215], v[26:27]
	v_pk_fma_f32 v[164:165], v[26:27], v[26:27], v[164:165]
	v_pk_add_f32 v[204:205], v[204:205], v[28:29]
	v_pk_fma_f32 v[162:163], v[28:29], v[28:29], v[162:163]
	v_cvt_pk_f16_f32 v252, v30, v31
	v_cvt_pk_f16_f32 v253, v32, v33
	ds_write_b64 v251, v[252:253] offset:4656
	v_pk_add_f32 v[202:203], v[202:203], v[30:31]
	v_pk_fma_f32 v[160:161], v[30:31], v[30:31], v[160:161]
	v_pk_add_f32 v[196:197], v[196:197], v[32:33]
	v_pk_fma_f32 v[156:157], v[32:33], v[32:33], v[156:157]
	s_nop 7
	s_waitcnt lgkmcnt(0)
	s_barrier
	s_nop 1
	ds_read_b128 v[16:19], v159 offset:43520
	s_waitcnt lgkmcnt(0)
	v_mfma_f32_32x32x16_f16 v[32:47], v[16:19], v[126:129], 0
	ds_read_b128 v[2:5], v159 offset:34816
	s_waitcnt lgkmcnt(0)
	v_mfma_f32_32x32x16_f16 v[48:63], v[2:5], v[126:129], 0
	ds_read_b128 v[126:129], v159 offset:34848
	s_waitcnt lgkmcnt(0)
	v_mfma_f32_32x32x16_f16 v[48:63], v[126:129], v[118:121], v[48:63]
	v_mfma_f32_32x32x16_f16 v[0:15], v[122:125], v[2:5], v[168:183]
	v_mfma_f32_32x32x16_f16 v[0:15], v[114:117], v[126:129], v[0:15]
	v_mfma_f32_32x32x16_f16 v[16:31], v[122:125], v[16:19], v[168:183]
	ds_read_b128 v[122:125], v159 offset:43552
	s_waitcnt lgkmcnt(0)
	v_mfma_f32_32x32x16_f16 v[32:47], v[122:125], v[118:121], v[32:47]
	v_mfma_f32_32x32x16_f16 v[16:31], v[114:117], v[122:125], v[16:31]
	ds_read_b128 v[118:121], v159 offset:34880
	ds_read_b128 v[114:117], v159 offset:43584
	s_waitcnt lgkmcnt(1)
	v_mfma_f32_32x32x16_f16 v[48:63], v[118:121], v[110:113], v[48:63]
	s_waitcnt lgkmcnt(0)
	v_mfma_f32_32x32x16_f16 v[32:47], v[114:117], v[110:113], v[32:47]
	v_mfma_f32_32x32x16_f16 v[0:15], v[106:109], v[118:121], v[0:15]
	ds_read_b128 v[110:113], v159 offset:34912
	v_mfma_f32_32x32x16_f16 v[16:31], v[106:109], v[114:117], v[16:31]
	ds_read_b128 v[106:109], v159 offset:43616
	s_waitcnt lgkmcnt(1)
	v_mfma_f32_32x32x16_f16 v[48:63], v[110:113], v[102:105], v[48:63]
	s_waitcnt lgkmcnt(0)
	v_mfma_f32_32x32x16_f16 v[32:47], v[106:109], v[102:105], v[32:47]
	v_mfma_f32_32x32x16_f16 v[0:15], v[98:101], v[110:113], v[0:15]
	ds_read_b128 v[102:105], v159 offset:34944
	v_mfma_f32_32x32x16_f16 v[16:31], v[98:101], v[106:109], v[16:31]
	ds_read_b128 v[98:101], v159 offset:43648
	s_waitcnt lgkmcnt(1)
	v_mfma_f32_32x32x16_f16 v[48:63], v[102:105], v[94:97], v[48:63]
	s_waitcnt lgkmcnt(0)
	v_mfma_f32_32x32x16_f16 v[32:47], v[98:101], v[94:97], v[32:47]
	v_mfma_f32_32x32x16_f16 v[0:15], v[86:89], v[102:105], v[0:15]
	ds_read_b128 v[94:97], v159 offset:34976
	v_mfma_f32_32x32x16_f16 v[16:31], v[86:89], v[98:101], v[16:31]
	ds_read_b128 v[86:89], v159 offset:43680
	s_waitcnt lgkmcnt(1)
	v_mfma_f32_32x32x16_f16 v[48:63], v[94:97], v[90:93], v[48:63]
	s_waitcnt lgkmcnt(0)
	v_mfma_f32_32x32x16_f16 v[32:47], v[86:89], v[90:93], v[32:47]
	v_mfma_f32_32x32x16_f16 v[0:15], v[78:81], v[94:97], v[0:15]
	ds_read_b128 v[90:93], v159 offset:35008
	v_mfma_f32_32x32x16_f16 v[16:31], v[78:81], v[86:89], v[16:31]
	ds_read_b128 v[78:81], v159 offset:43712
	s_waitcnt lgkmcnt(1)
	v_mfma_f32_32x32x16_f16 v[48:63], v[90:93], v[82:85], v[48:63]
	s_waitcnt lgkmcnt(0)
	v_mfma_f32_32x32x16_f16 v[32:47], v[78:81], v[82:85], v[32:47]
	v_mfma_f32_32x32x16_f16 v[0:15], v[70:73], v[90:93], v[0:15]
	ds_read_b128 v[82:85], v159 offset:35040
	v_mfma_f32_32x32x16_f16 v[16:31], v[70:73], v[78:81], v[16:31]
	ds_read_b128 v[70:73], v159 offset:43744
	s_waitcnt lgkmcnt(1)
	v_mfma_f32_32x32x16_f16 v[48:63], v[82:85], v[74:77], v[48:63]
	v_mfma_f32_32x32x16_f16 v[0:15], v[66:69], v[82:85], v[0:15]
	s_nop 3
	s_nop 6
	v_cvt_pk_f16_f32 v55, v54, v55
	v_cvt_pk_f16_f32 v54, v52, v53
	v_cvt_pk_f16_f32 v53, v50, v51
	v_cvt_pk_f16_f32 v52, v48, v49
	s_waitcnt vmcnt(3)
	s_waitcnt lgkmcnt(0)
	v_mfma_f32_32x32x16_f16 v[16:31], v[66:69], v[70:73], v[16:31]
	v_lshrrev_b32_e32 v69, 16, v139
	v_mfma_f32_32x32x16_f16 v[32:47], v[70:73], v[74:77], v[32:47]
	v_lshrrev_b32_e32 v70, 8, v139
	v_perm_b32 v69, v70, v69, s2
	v_perm_b32 v66, v240, v138, s42
	v_perm_b32 v67, v240, v138, s43
	v_perm_b32 v68, v240, v139, s42
	v_or_b32_e32 v69, 0x64006400, v69
	v_pk_add_f16 v66, v66, s3 op_sel_hi:[1,0]
	v_pk_add_f16 v67, v67, s3 op_sel_hi:[1,0]
	v_pk_add_f16 v68, v68, s3 op_sel_hi:[1,0]
	v_pk_add_f16 v69, v69, s3 op_sel_hi:[1,0]
	s_nop 1
	v_mfma_f32_32x32x16_f16 v[0:15], v[52:55], v[66:69], v[0:15]
	v_perm_b32 v48, v240, v136, s42
	v_perm_b32 v49, v240, v136, s43
	v_perm_b32 v50, v240, v137, s42
	v_perm_b32 v51, v240, v137, s43
	v_pk_add_f16 v48, v48, s3 op_sel_hi:[1,0]
	v_pk_add_f16 v49, v49, s3 op_sel_hi:[1,0]
	v_pk_add_f16 v50, v50, s3 op_sel_hi:[1,0]
	v_pk_add_f16 v51, v51, s3 op_sel_hi:[1,0]
	v_cvt_pk_f16_f32 v39, v38, v39
	v_cvt_pk_f16_f32 v38, v36, v37
	v_mfma_f32_32x32x16_f16 v[16:31], v[52:55], v[48:51], v[16:31]
	v_perm_b32 v48, v240, v134, s42
	v_perm_b32 v49, v240, v134, s43
	v_perm_b32 v50, v240, v135, s42
	v_perm_b32 v51, v240, v135, s43
	v_pk_add_f16 v48, v48, s3 op_sel_hi:[1,0]
	v_pk_add_f16 v49, v49, s3 op_sel_hi:[1,0]
	v_pk_add_f16 v50, v50, s3 op_sel_hi:[1,0]
	v_pk_add_f16 v51, v51, s3 op_sel_hi:[1,0]
	v_cvt_pk_f16_f32 v55, v62, v63
	v_cvt_pk_f16_f32 v54, v60, v61
	v_cvt_pk_f16_f32 v53, v58, v59
	v_cvt_pk_f16_f32 v52, v56, v57
	s_waitcnt vmcnt(2)
	v_cvt_pk_f16_f32 v37, v34, v35
	v_mfma_f32_32x32x16_f16 v[0:15], v[52:55], v[48:51], v[0:15]
	v_perm_b32 v48, v240, v142, s42
	v_perm_b32 v49, v240, v142, s43
	v_perm_b32 v50, v240, v143, s42
	v_perm_b32 v51, v240, v143, s43
	v_pk_add_f16 v48, v48, s3 op_sel_hi:[1,0]
	v_pk_add_f16 v49, v49, s3 op_sel_hi:[1,0]
	v_pk_add_f16 v50, v50, s3 op_sel_hi:[1,0]
	v_pk_add_f16 v51, v51, s3 op_sel_hi:[1,0]
	v_cvt_pk_f16_f32 v36, v32, v33
	s_waitcnt vmcnt(1)
	v_mfma_f32_32x32x16_f16 v[16:31], v[52:55], v[48:51], v[16:31]
	v_lshrrev_b32_e32 v51, 16, v133
	v_lshrrev_b32_e32 v52, 8, v133
	v_perm_b32 v51, v52, v51, s2
	v_perm_b32 v48, v240, v132, s42
	v_perm_b32 v49, v240, v132, s43
	v_perm_b32 v50, v240, v133, s42
	v_or_b32_e32 v51, 0x64006400, v51
	v_pk_add_f16 v48, v48, s3 op_sel_hi:[1,0]
	v_pk_add_f16 v49, v49, s3 op_sel_hi:[1,0]
	v_pk_add_f16 v50, v50, s3 op_sel_hi:[1,0]
	v_pk_add_f16 v51, v51, s3 op_sel_hi:[1,0]
	s_nop 1
	v_mfma_f32_32x32x16_f16 v[0:15], v[36:39], v[48:51], v[0:15]
	v_perm_b32 v32, v240, v140, s42
	v_perm_b32 v33, v240, v140, s43
	v_perm_b32 v34, v240, v141, s42
	v_perm_b32 v35, v240, v141, s43
	v_pk_add_f16 v32, v32, s3 op_sel_hi:[1,0]
	v_pk_add_f16 v33, v33, s3 op_sel_hi:[1,0]
	v_pk_add_f16 v34, v34, s3 op_sel_hi:[1,0]
	v_pk_add_f16 v35, v35, s3 op_sel_hi:[1,0]
	s_nop 1
	v_mfma_f32_32x32x16_f16 v[16:31], v[36:39], v[32:35], v[16:31]
	v_perm_b32 v32, v240, v130, s42
	v_perm_b32 v33, v240, v130, s43
	v_perm_b32 v34, v240, v131, s42
	v_perm_b32 v35, v240, v131, s43
	v_pk_add_f16 v32, v32, s3 op_sel_hi:[1,0]
	v_pk_add_f16 v33, v33, s3 op_sel_hi:[1,0]
	v_pk_add_f16 v34, v34, s3 op_sel_hi:[1,0]
	v_pk_add_f16 v35, v35, s3 op_sel_hi:[1,0]
	v_cvt_pk_f16_f32 v39, v46, v47
	v_cvt_pk_f16_f32 v38, v44, v45
	v_cvt_pk_f16_f32 v37, v42, v43
	v_cvt_pk_f16_f32 v36, v40, v41
	s_waitcnt vmcnt(0)
	s_nop 0
	v_mfma_f32_32x32x16_f16 v[0:15], v[36:39], v[32:35], v[0:15]
	v_perm_b32 v32, v240, v64, s42
	v_perm_b32 v33, v240, v64, s43
	v_perm_b32 v34, v240, v65, s42
	v_perm_b32 v35, v240, v65, s43
	v_pk_add_f16 v32, v32, s3 op_sel_hi:[1,0]
	v_pk_add_f16 v33, v33, s3 op_sel_hi:[1,0]
	v_pk_add_f16 v34, v34, s3 op_sel_hi:[1,0]
	v_pk_add_f16 v35, v35, s3 op_sel_hi:[1,0]
	s_nop 3
	v_mfma_f32_32x32x16_f16 v[16:31], v[36:39], v[32:35], v[16:31]
	s_nop 7
	s_nop 4
	v_cvt_pk_f16_f32 v254, v0, v1
	v_cvt_pk_f16_f32 v255, v2, v3
	ds_write_b64 v251, v[254:255] offset:18432
	v_pk_add_f32 v[222:223], v[222:223], v[0:1]
	v_pk_fma_f32 v[194:195], v[0:1], v[0:1], v[194:195]
	v_pk_add_f32 v[220:221], v[220:221], v[2:3]
	v_pk_fma_f32 v[192:193], v[2:3], v[2:3], v[192:193]
	v_cvt_pk_f16_f32 v252, v4, v5
	v_cvt_pk_f16_f32 v253, v6, v7
	ds_write_b64 v251, v[252:253] offset:18448
	v_pk_add_f32 v[218:219], v[218:219], v[4:5]
	v_pk_fma_f32 v[184:185], v[4:5], v[4:5], v[184:185]
	v_pk_add_f32 v[216:217], v[216:217], v[6:7]
	v_pk_fma_f32 v[166:167], v[6:7], v[6:7], v[166:167]
	v_cvt_pk_f16_f32 v254, v8, v9
	v_cvt_pk_f16_f32 v255, v10, v11
	ds_write_b64 v251, v[254:255] offset:18464
	v_pk_add_f32 v[214:215], v[214:215], v[8:9]
	v_pk_fma_f32 v[164:165], v[8:9], v[8:9], v[164:165]
	v_pk_add_f32 v[204:205], v[204:205], v[10:11]
	v_pk_fma_f32 v[162:163], v[10:11], v[10:11], v[162:163]
	v_cvt_pk_f16_f32 v252, v12, v13
	v_cvt_pk_f16_f32 v253, v14, v15
	ds_write_b64 v251, v[252:253] offset:18480
	v_pk_add_f32 v[202:203], v[202:203], v[12:13]
	v_pk_fma_f32 v[160:161], v[12:13], v[12:13], v[160:161]
	v_pk_add_f32 v[196:197], v[196:197], v[14:15]
	v_pk_fma_f32 v[156:157], v[14:15], v[14:15], v[156:157]
	v_cvt_pk_f16_f32 v254, v16, v17
	v_cvt_pk_f16_f32 v255, v18, v19
	ds_write_b64 v251, v[254:255] offset:23040
	v_pk_add_f32 v[222:223], v[222:223], v[16:17]
	v_pk_fma_f32 v[194:195], v[16:17], v[16:17], v[194:195]
	v_pk_add_f32 v[220:221], v[220:221], v[18:19]
	v_pk_fma_f32 v[192:193], v[18:19], v[18:19], v[192:193]
	v_cvt_pk_f16_f32 v252, v20, v21
	v_cvt_pk_f16_f32 v253, v22, v23
	ds_write_b64 v251, v[252:253] offset:23056
	v_pk_add_f32 v[218:219], v[218:219], v[20:21]
	v_pk_fma_f32 v[184:185], v[20:21], v[20:21], v[184:185]
	v_pk_add_f32 v[216:217], v[216:217], v[22:23]
	v_pk_fma_f32 v[166:167], v[22:23], v[22:23], v[166:167]
	v_cvt_pk_f16_f32 v254, v24, v25
	v_cvt_pk_f16_f32 v255, v26, v27
	ds_write_b64 v251, v[254:255] offset:23072
	v_pk_add_f32 v[214:215], v[214:215], v[24:25]
	v_pk_fma_f32 v[164:165], v[24:25], v[24:25], v[164:165]
	v_pk_add_f32 v[204:205], v[204:205], v[26:27]
	v_pk_fma_f32 v[162:163], v[26:27], v[26:27], v[162:163]
	v_cvt_pk_f16_f32 v252, v28, v29
	v_cvt_pk_f16_f32 v253, v30, v31
	ds_write_b64 v251, v[252:253] offset:23088
	v_pk_add_f32 v[202:203], v[202:203], v[28:29]
	v_pk_fma_f32 v[160:161], v[28:29], v[28:29], v[160:161]
	v_pk_add_f32 v[196:197], v[196:197], v[30:31]
	v_pk_fma_f32 v[156:157], v[30:31], v[30:31], v[156:157]
	s_nop 4
	s_nop 0
	v_add_f32_dpp v222, v222, v222 row_half_mirror row_mask:0xf bank_mask:0x5
	v_add_f32_dpp v222, v223, v223 row_half_mirror row_mask:0xf bank_mask:0xa
	v_add_f32_dpp v220, v220, v220 row_half_mirror row_mask:0xf bank_mask:0x5
	v_add_f32_dpp v220, v221, v221 row_half_mirror row_mask:0xf bank_mask:0xa
	v_add_f32_dpp v218, v218, v218 row_half_mirror row_mask:0xf bank_mask:0x5
	v_add_f32_dpp v218, v219, v219 row_half_mirror row_mask:0xf bank_mask:0xa
	v_add_f32_dpp v216, v216, v216 row_half_mirror row_mask:0xf bank_mask:0x5
	v_add_f32_dpp v216, v217, v217 row_half_mirror row_mask:0xf bank_mask:0xa
	v_add_f32_dpp v214, v214, v214 row_half_mirror row_mask:0xf bank_mask:0x5
	v_add_f32_dpp v214, v215, v215 row_half_mirror row_mask:0xf bank_mask:0xa
	v_add_f32_dpp v204, v204, v204 row_half_mirror row_mask:0xf bank_mask:0x5
	v_add_f32_dpp v204, v205, v205 row_half_mirror row_mask:0xf bank_mask:0xa
	v_add_f32_dpp v202, v202, v202 row_half_mirror row_mask:0xf bank_mask:0x5
	v_add_f32_dpp v202, v203, v203 row_half_mirror row_mask:0xf bank_mask:0xa
	v_add_f32_dpp v196, v196, v196 row_half_mirror row_mask:0xf bank_mask:0x5
	v_add_f32_dpp v196, v197, v197 row_half_mirror row_mask:0xf bank_mask:0xa
	v_add_f32_dpp v194, v194, v194 row_half_mirror row_mask:0xf bank_mask:0x5
	v_add_f32_dpp v194, v195, v195 row_half_mirror row_mask:0xf bank_mask:0xa
	v_add_f32_dpp v192, v192, v192 row_half_mirror row_mask:0xf bank_mask:0x5
	v_add_f32_dpp v192, v193, v193 row_half_mirror row_mask:0xf bank_mask:0xa
	v_add_f32_dpp v184, v184, v184 row_half_mirror row_mask:0xf bank_mask:0x5
	v_add_f32_dpp v184, v185, v185 row_half_mirror row_mask:0xf bank_mask:0xa
	v_add_f32_dpp v166, v166, v166 row_half_mirror row_mask:0xf bank_mask:0x5
	v_add_f32_dpp v166, v167, v167 row_half_mirror row_mask:0xf bank_mask:0xa
	v_add_f32_dpp v164, v164, v164 row_half_mirror row_mask:0xf bank_mask:0x5
	v_add_f32_dpp v164, v165, v165 row_half_mirror row_mask:0xf bank_mask:0xa
	v_add_f32_dpp v162, v162, v162 row_half_mirror row_mask:0xf bank_mask:0x5
	v_add_f32_dpp v162, v163, v163 row_half_mirror row_mask:0xf bank_mask:0xa
	v_add_f32_dpp v160, v160, v160 row_half_mirror row_mask:0xf bank_mask:0x5
	v_add_f32_dpp v160, v161, v161 row_half_mirror row_mask:0xf bank_mask:0xa
	v_add_f32_dpp v156, v156, v156 row_half_mirror row_mask:0xf bank_mask:0x5
	v_add_f32_dpp v156, v157, v157 row_half_mirror row_mask:0xf bank_mask:0xa
	v_add_f32_dpp v222, v222, v222 row_ror:8 row_mask:0xf bank_mask:0x3
	v_add_f32_dpp v222, v220, v220 row_ror:8 row_mask:0xf bank_mask:0xc
	v_add_f32_dpp v218, v218, v218 row_ror:8 row_mask:0xf bank_mask:0x3
	v_add_f32_dpp v218, v216, v216 row_ror:8 row_mask:0xf bank_mask:0xc
	v_add_f32_dpp v214, v214, v214 row_ror:8 row_mask:0xf bank_mask:0x3
	v_add_f32_dpp v214, v204, v204 row_ror:8 row_mask:0xf bank_mask:0xc
	v_add_f32_dpp v202, v202, v202 row_ror:8 row_mask:0xf bank_mask:0x3
	v_add_f32_dpp v202, v196, v196 row_ror:8 row_mask:0xf bank_mask:0xc
	v_add_f32_dpp v194, v194, v194 row_ror:8 row_mask:0xf bank_mask:0x3
	v_add_f32_dpp v194, v192, v192 row_ror:8 row_mask:0xf bank_mask:0xc
	v_add_f32_dpp v184, v184, v184 row_ror:8 row_mask:0xf bank_mask:0x3
	v_add_f32_dpp v184, v166, v166 row_ror:8 row_mask:0xf bank_mask:0xc
	v_add_f32_dpp v164, v164, v164 row_ror:8 row_mask:0xf bank_mask:0x3
	v_add_f32_dpp v164, v162, v162 row_ror:8 row_mask:0xf bank_mask:0xc
	v_add_f32_dpp v160, v160, v160 row_ror:8 row_mask:0xf bank_mask:0x3
	v_add_f32_dpp v160, v156, v156 row_ror:8 row_mask:0xf bank_mask:0xc
	v_add_f32_dpp v222, v222, v222 quad_perm:[1,0,3,2] row_mask:0xf bank_mask:0xf
	v_add_f32_dpp v218, v218, v218 quad_perm:[1,0,3,2] row_mask:0xf bank_mask:0xf
	v_add_f32_dpp v214, v214, v214 quad_perm:[1,0,3,2] row_mask:0xf bank_mask:0xf
	v_add_f32_dpp v202, v202, v202 quad_perm:[1,0,3,2] row_mask:0xf bank_mask:0xf
	v_add_f32_dpp v194, v194, v194 quad_perm:[1,0,3,2] row_mask:0xf bank_mask:0xf
	v_add_f32_dpp v184, v184, v184 quad_perm:[1,0,3,2] row_mask:0xf bank_mask:0xf
	v_add_f32_dpp v164, v164, v164 quad_perm:[1,0,3,2] row_mask:0xf bank_mask:0xf
	v_add_f32_dpp v160, v160, v160 quad_perm:[1,0,3,2] row_mask:0xf bank_mask:0xf
	v_add_f32_dpp v222, v222, v222 quad_perm:[2,3,0,1] row_mask:0xf bank_mask:0xf
	v_add_f32_dpp v218, v218, v218 quad_perm:[2,3,0,1] row_mask:0xf bank_mask:0xf
	v_add_f32_dpp v214, v214, v214 quad_perm:[2,3,0,1] row_mask:0xf bank_mask:0xf
	v_add_f32_dpp v202, v202, v202 quad_perm:[2,3,0,1] row_mask:0xf bank_mask:0xf
	v_add_f32_dpp v194, v194, v194 quad_perm:[2,3,0,1] row_mask:0xf bank_mask:0xf
	v_add_f32_dpp v184, v184, v184 quad_perm:[2,3,0,1] row_mask:0xf bank_mask:0xf
	v_add_f32_dpp v164, v164, v164 quad_perm:[2,3,0,1] row_mask:0xf bank_mask:0xf
	v_add_f32_dpp v160, v160, v160 quad_perm:[2,3,0,1] row_mask:0xf bank_mask:0xf
	s_mov_b32 exec_lo, 0x11111111
	s_mov_b32 exec_hi, 0x11111111
	ds_add_f32 v250, v222 offset:0
	ds_add_f32 v250, v218 offset:32
	ds_add_f32 v250, v214 offset:64
	ds_add_f32 v250, v202 offset:96
	ds_add_f32 v250, v194 offset:256
	ds_add_f32 v250, v184 offset:288
	ds_add_f32 v250, v164 offset:320
	ds_add_f32 v250, v160 offset:352
	s_mov_b64 exec, -1
	s_waitcnt lgkmcnt(0)
	s_barrier
	s_cmp_lg_u32 s50, 0
	s_cbranch_scc1 .LBB3_27
	v_mbcnt_lo_u32_b32 v2, -1, 0
	v_mbcnt_hi_u32_b32 v2, -1, v2
	v_and_b32_e32 v3, 32, v2
	v_add_u32_e32 v4, v2, v3
	v_lshl_add_u32 v5, v4, 2, s49
	ds_read_b32 v6, v5
	v_lshl_add_u32 v4, v3, 1, v4
	v_add_u32_e32 v4, s48, v4
	v_lshlrev_b32_e32 v4, 2, v4
	s_waitcnt lgkmcnt(0)
	global_atomic_add_f32 v4, v6, s[46:47]
